# memory cross-attention unit: the eight query-fragment row gathers are issued before the K/V staging loop instead of after it (same loads, earlier)
# baseline (speedup 1.0000x reference)
; #define LAS __attribute__((address_space(3)))
; __device__ __forceinline__ void memattn_unit(LAS unsigned char* lds, const bf16* PROJ, const bf16* MKVl, bf16* BR, int b, int hd, int qblk, int tid) {
;     asm volatile("" : "+v"(tid));
;     const int lane = tid & 63, wave = __builtin_amdgcn_readfirstlane(tid >> 6), r = lane & 31, hh = lane >> 5;
;     LAS unsigned char* kimg = lds; LAS unsigned char* vimg = lds + 65536;
;     { const bf16* kb = MKVl + (size_t)b * 256 * 1024 + hd * 128;
; #pragma unroll 4
;       for (int it = 0; it < 8; ++it) { const int row = it * 32 + (tid >> 4), ch = tid & 15;
;           const v4u kv = *(const v4u*)(kb + (size_t)row * 1024 + ch * 8), vv = *(const v4u*)(kb + (size_t)row * 1024 + 512 + ch * 8);
;           *(LAS v4u*)(kimg + kv_off(row, ch)) = kv; *(LAS v4u*)(vimg + kv_off(row, ch)) = vv; } }
;     const size_t tok = (size_t)b * T + qblk * 256 + wave * 32 + r;
;     bf16x8 qf[8];
; #pragma unroll
;     for (int s = 0; s < 8; ++s) qf[s] = *(const bf16x8*)(PROJ + tok * NP + PC_MQ + hd * 128 + 16 * s + 8 * hh);
.LBB0_599:
	s_ashr_i32 s0, s7, 31
	s_lshr_b32 s1, s0, 27
	s_lshr_b32 s0, s0, 25
	s_add_i32 s1, s7, s1
	s_add_i32 s0, s7, s0
	s_ashr_i32 s6, s1, 5
	s_ashr_i32 s0, s0, 7
	s_ashr_i32 s1, s0, 31
	s_lshl_b32 s10, s6, 8
	s_lshl_b64 s[8:9], s[0:1], 19
	s_and_b32 s22, s10, 0x300
	v_mov_b32_e32 v162, v129
	s_add_u32 s10, s2, s22
	s_addc_u32 s11, s3, 0
	v_ashrrev_i32_e32 v0, 4, v162
	v_ashrrev_i32_e32 v1, 31, v0
	s_add_u32 s8, s10, s8
	v_and_b32_e32 v12, 15, v162
	v_bfe_u32 v13, v0, 2, 2
	v_lshlrev_b32_e32 v14, 2, v0
	v_lshl_add_u32 v15, v0, 8, s14
	v_lshlrev_b64 v[0:1], 11, v[0:1]
	s_addc_u32 s9, s11, s9
	v_lshlrev_b32_e32 v8, 4, v12
	v_mov_b32_e32 v9, v128
	v_lshl_add_u64 v[10:11], s[8:9], 0, v[0:1]
	s_lshl_b32 s6, s6, 5
	s_sub_i32 s6, s7, s6
	s_lshl_b32 s6, s6, 8
	s_lshl_b64 s[0:1], s[0:1], 13
	s_ashr_i32 s9, s6, 31
	v_readfirstlane_b32 s8, v162
	s_add_u32 s6, s0, s6
	s_addc_u32 s9, s1, s9
	s_ashr_i32 s0, s8, 1
	s_andn2_b32 s0, s0, 31
	s_ashr_i32 s1, s0, 31
	v_and_or_b32 v0, v162, 31, s6
	v_mov_b32_e32 v1, s9
	v_lshl_add_u64 v[158:159], v[0:1], 0, s[0:1]
	v_lshlrev_b64 v[0:1], 14, v[158:159]
	v_bfe_u32 v163, v162, 5, 1
	v_lshl_add_u64 v[0:1], s[4:5], 0, v[0:1]
	v_lshl_add_u64 v[0:1], v[0:1], 0, s[22:23]
	v_lshlrev_b32_e32 v2, 4, v163
	v_mov_b32_e32 v3, v128
	v_lshl_add_u64 v[0:1], v[0:1], 0, v[2:3]
	s_movk_i32 s0, 0x1000
	v_add_co_u32_e32 v2, vcc, s0, v0
	s_mov_b64 s[0:1], 0x1c00
	s_nop 0
	v_addc_co_u32_e32 v3, vcc, 0, v1, vcc
	global_load_dwordx4 v[112:115], v[2:3], off offset:3072
	v_lshl_add_u64 v[0:1], v[0:1], 0, s[0:1]
	global_load_dwordx4 v[130:133], v[0:1], off offset:32
	global_load_dwordx4 v[134:137], v[0:1], off offset:64
	global_load_dwordx4 v[138:141], v[0:1], off offset:96
	global_load_dwordx4 v[146:149], v[0:1], off offset:128
	global_load_dwordx4 v[150:153], v[0:1], off offset:160
	global_load_dwordx4 v[154:157], v[0:1], off offset:192
	global_load_dwordx4 v[142:145], v[0:1], off offset:224
	s_mov_b32 s8, 0
.LBB0_600:
	v_lshl_add_u64 v[32:33], v[10:11], 0, v[8:9]
	v_add_co_u32_e32 v4, vcc, 0x36a00000, v32
	v_add_u32_e32 v41, 0x80, v14
	s_nop 0
	v_addc_co_u32_e32 v5, vcc, 0, v33, vcc
	v_add_co_u32_e32 v20, vcc, 0x36a10000, v32
	global_load_dwordx4 v[0:3], v[4:5], off
	s_nop 0
	global_load_dwordx4 v[4:7], v[4:5], off offset:1024
	v_addc_co_u32_e32 v21, vcc, 0, v33, vcc
	v_add_co_u32_e32 v28, vcc, 0x36a20000, v32
	global_load_dwordx4 v[16:19], v[20:21], off
	s_nop 0
	global_load_dwordx4 v[20:23], v[20:21], off offset:1024
	v_addc_co_u32_e32 v29, vcc, 0, v33, vcc
	v_add_co_u32_e32 v36, vcc, 0x36a30000, v32
	global_load_dwordx4 v[24:27], v[28:29], off
	s_nop 0
	global_load_dwordx4 v[28:31], v[28:29], off offset:1024
	v_addc_co_u32_e32 v37, vcc, 0, v33, vcc
	global_load_dwordx4 v[32:35], v[36:37], off
	s_nop 0
	global_load_dwordx4 v[36:39], v[36:37], off offset:1024
	v_add_u32_e32 v42, 0x100, v14
	v_add_u32_e32 v43, 0x180, v14
	v_and_b32_e32 v40, 12, v14
	v_and_b32_e32 v41, 12, v41
	v_and_b32_e32 v42, 12, v42
	v_and_b32_e32 v43, 12, v43
	v_bitop3_b32 v40, v40, v12, v13 bitop3:0x36
	v_bitop3_b32 v41, v41, v12, v13 bitop3:0x36
	v_bitop3_b32 v42, v42, v12, v13 bitop3:0x36
	v_bitop3_b32 v43, v43, v12, v13 bitop3:0x36
	v_lshlrev_b32_e32 v40, 4, v40
	v_lshlrev_b32_e32 v41, 4, v41
	v_lshlrev_b32_e32 v42, 4, v42
	v_lshlrev_b32_e32 v43, 4, v43
	v_add3_u32 v40, v15, v40, s8
	v_add3_u32 v41, v15, v41, s8
	v_add3_u32 v42, v15, v42, s8
	v_add3_u32 v43, v15, v43, s8
	s_add_i32 s8, s8, 0x8000
	v_add_u32_e32 v14, 0x200, v14
	v_lshl_add_u64 v[10:11], v[10:11], 0, s[12:13]
	s_cmp_lg_u32 s8, 0x10000
	v_add_u32_e32 v44, 0x10000, v40
	v_add_u32_e32 v45, 0x12000, v41
	v_add_u32_e32 v46, 0x14000, v42
	v_add_u32_e32 v47, 0x16000, v43
	s_waitcnt vmcnt(7)
	ds_write_b128 v40, v[0:3]
	s_waitcnt vmcnt(6)
	ds_write_b128 v44, v[4:7]
	s_waitcnt vmcnt(5)
	ds_write_b128 v41, v[16:19] offset:8192
	s_waitcnt vmcnt(4)
	ds_write_b128 v45, v[20:23]
	s_waitcnt vmcnt(3)
	ds_write_b128 v42, v[24:27] offset:16384
	s_waitcnt vmcnt(2)
	ds_write_b128 v46, v[28:31]
	s_waitcnt vmcnt(1)
	ds_write_b128 v43, v[32:35] offset:24576
	s_waitcnt vmcnt(0)
	ds_write_b128 v47, v[36:39]
	s_cbranch_scc1 .LBB0_600
	v_lshrrev_b32_e32 v3, 1, v162
	v_lshlrev_b32_e32 v2, 1, v162
	v_and_b32_e32 v3, 4, v3
	v_lshlrev_b32_e32 v4, 2, v162
	v_and_or_b32 v2, v2, 8, v3
	v_and_b32_e32 v40, 12, v4
	v_and_or_b32 v3, v162, 19, v2
	v_lshrrev_b32_e32 v41, 2, v2
	v_lshl_add_u32 v42, v3, 8, s14
	v_bitop3_b32 v2, v41, v163, v40 bitop3:0x36
	v_lshl_add_u32 v96, v2, 4, v42
	s_waitcnt lgkmcnt(0)
	s_barrier
; #define LAS __attribute__((address_space(3)))
; __device__ __forceinline__ unsigned swap23(unsigned r) { return (r & ~12u) | ((r & 4u) << 1) | ((r & 8u) >> 1); }
; __device__ __forceinline__ void memattn_unit(LAS unsigned char* lds, const bf16* PROJ, const bf16* MKVl, bf16* BR, int b, int hd, int qblk, int tid) {
;     ...
;     f32x16 S[8];
; #pragma unroll
;     for (int kap = 0; kap < 8; ++kap) { f32x16 acc;
; #pragma unroll
;         for (int i = 0; i < 16; ++i) acc[i] = 0.f;
;         const unsigned slot = 32u * kap + swap23((unsigned)r);
; #pragma unroll
;         for (int s = 0; s < 8; ++s) { const bf16x8 a = *(const LAS bf16x8*)(kimg + kv_off(slot, 2 * s + hh)); acc = __builtin_amdgcn_mfma_f32_32x32x16_bf16(a, qf[s], acc, 0, 0, 0); }
;         S[kap] = acc; if (kap & 1) __builtin_amdgcn_sched_barrier(0); }
	ds_read_b128 v[0:3], v96
	ds_read_b128 v[4:7], v96 offset:8192
	v_mov_b32_e32 v161, v128
	v_lshlrev_b32_e32 v160, 3, v163
	s_waitcnt vmcnt(7) lgkmcnt(1)
	v_mfma_f32_32x32x16_bf16 v[16:31], v[0:3], v[112:115], 0
	v_or_b32_e32 v0, 2, v163
	v_bitop3_b32 v0, v41, v0, v40 bitop3:0x36
	v_lshl_add_u32 v116, v0, 4, v42
	ds_read_b128 v[32:35], v116
	ds_read_b128 v[36:39], v116 offset:8192
	s_waitcnt lgkmcnt(2)
	v_mfma_f32_32x32x16_bf16 v[0:15], v[4:7], v[112:115], 0
	s_waitcnt vmcnt(6) lgkmcnt(1)
	v_mfma_f32_32x32x16_bf16 v[16:31], v[32:35], v[130:133], v[16:31]
	v_or_b32_e32 v32, 4, v163
	v_bitop3_b32 v32, v41, v32, v40 bitop3:0x36
	v_lshl_add_u32 v117, v32, 4, v42
	s_waitcnt lgkmcnt(0)
	v_mfma_f32_32x32x16_bf16 v[0:15], v[36:39], v[130:133], v[0:15]
	ds_read_b128 v[32:35], v117
	ds_read_b128 v[36:39], v117 offset:8192
	s_waitcnt vmcnt(5) lgkmcnt(1)
	v_mfma_f32_32x32x16_bf16 v[16:31], v[32:35], v[134:137], v[16:31]
	v_or_b32_e32 v32, 6, v163
	v_bitop3_b32 v32, v41, v32, v40 bitop3:0x36
	v_lshl_add_u32 v118, v32, 4, v42
	s_waitcnt lgkmcnt(0)
	v_mfma_f32_32x32x16_bf16 v[0:15], v[36:39], v[134:137], v[0:15]
	ds_read_b128 v[32:35], v118
	ds_read_b128 v[36:39], v118 offset:8192
	s_waitcnt vmcnt(4) lgkmcnt(1)
	v_mfma_f32_32x32x16_bf16 v[16:31], v[32:35], v[138:141], v[16:31]
	v_or_b32_e32 v32, 8, v163
	v_bitop3_b32 v32, v41, v32, v40 bitop3:0x36
	v_lshl_add_u32 v119, v32, 4, v42
	s_waitcnt lgkmcnt(0)
	v_mfma_f32_32x32x16_bf16 v[0:15], v[36:39], v[138:141], v[0:15]
	ds_read_b128 v[32:35], v119
	ds_read_b128 v[36:39], v119 offset:8192
	s_waitcnt vmcnt(3) lgkmcnt(1)
	v_mfma_f32_32x32x16_bf16 v[16:31], v[32:35], v[146:149], v[16:31]
	v_or_b32_e32 v32, 10, v163
	v_bitop3_b32 v32, v41, v32, v40 bitop3:0x36
	v_lshl_add_u32 v180, v32, 4, v42
	s_waitcnt lgkmcnt(0)
	v_mfma_f32_32x32x16_bf16 v[0:15], v[36:39], v[146:149], v[0:15]
	ds_read_b128 v[32:35], v180
	ds_read_b128 v[36:39], v180 offset:8192
	s_waitcnt vmcnt(2) lgkmcnt(1)
	v_mfma_f32_32x32x16_bf16 v[16:31], v[32:35], v[150:153], v[16:31]
	v_or_b32_e32 v32, 12, v163
	v_bitop3_b32 v32, v41, v32, v40 bitop3:0x36
	v_lshl_add_u32 v184, v32, 4, v42
	s_waitcnt lgkmcnt(0)
	v_mfma_f32_32x32x16_bf16 v[0:15], v[36:39], v[150:153], v[0:15]
	ds_read_b128 v[32:35], v184
	ds_read_b128 v[36:39], v184 offset:8192
	s_waitcnt vmcnt(1) lgkmcnt(1)
	v_mfma_f32_32x32x16_bf16 v[16:31], v[32:35], v[154:157], v[16:31]
	v_or_b32_e32 v32, 14, v163
	v_bitop3_b32 v32, v41, v32, v40 bitop3:0x36
	v_lshl_add_u32 v188, v32, 4, v42
	s_waitcnt lgkmcnt(0)
	v_mfma_f32_32x32x16_bf16 v[0:15], v[36:39], v[154:157], v[0:15]
	ds_read_b128 v[32:35], v188
	ds_read_b128 v[36:39], v188 offset:8192
	s_waitcnt vmcnt(0) lgkmcnt(1)
	v_mfma_f32_32x32x16_bf16 v[16:31], v[32:35], v[142:145], v[16:31]
	s_waitcnt lgkmcnt(0)
	v_mfma_f32_32x32x16_bf16 v[0:15], v[36:39], v[142:145], v[0:15]
	ds_read_b128 v[32:35], v96 offset:16384
	ds_read_b128 v[48:51], v96 offset:24576
	ds_read_b128 v[52:55], v116 offset:16384
	ds_read_b128 v[64:67], v116 offset:24576
	s_waitcnt lgkmcnt(3)
	v_mfma_f32_32x32x16_bf16 v[32:47], v[32:35], v[112:115], 0
	s_waitcnt lgkmcnt(1)
	v_mfma_f32_32x32x16_bf16 v[32:47], v[52:55], v[130:133], v[32:47]
	ds_read_b128 v[52:55], v117 offset:16384
	ds_read_b128 v[68:71], v117 offset:24576
	s_waitcnt lgkmcnt(1)
	v_mfma_f32_32x32x16_bf16 v[32:47], v[52:55], v[134:137], v[32:47]
	ds_read_b128 v[52:55], v118 offset:16384
	ds_read_b128 v[72:75], v118 offset:24576
	s_waitcnt lgkmcnt(1)
	v_mfma_f32_32x32x16_bf16 v[32:47], v[52:55], v[138:141], v[32:47]
	ds_read_b128 v[52:55], v119 offset:16384
	ds_read_b128 v[76:79], v119 offset:24576
	s_waitcnt lgkmcnt(1)
	v_mfma_f32_32x32x16_bf16 v[32:47], v[52:55], v[146:149], v[32:47]
	ds_read_b128 v[52:55], v180 offset:16384
	ds_read_b128 v[80:83], v180 offset:24576
	s_waitcnt lgkmcnt(1)
	v_mfma_f32_32x32x16_bf16 v[32:47], v[52:55], v[150:153], v[32:47]
	ds_read_b128 v[52:55], v184 offset:16384
	ds_read_b128 v[84:87], v184 offset:24576
	s_waitcnt lgkmcnt(1)
	v_mfma_f32_32x32x16_bf16 v[32:47], v[52:55], v[154:157], v[32:47]
	ds_read_b128 v[52:55], v188 offset:16384
	ds_read_b128 v[88:91], v188 offset:24576
	s_waitcnt lgkmcnt(1)
	v_mfma_f32_32x32x16_bf16 v[32:47], v[52:55], v[142:145], v[32:47]
	v_mfma_f32_32x32x16_bf16 v[48:63], v[48:51], v[112:115], 0
	v_mfma_f32_32x32x16_bf16 v[48:63], v[64:67], v[130:133], v[48:63]
	v_mfma_f32_32x32x16_bf16 v[48:63], v[68:71], v[134:137], v[48:63]
	v_mfma_f32_32x32x16_bf16 v[48:63], v[72:75], v[138:141], v[48:63]
	v_mfma_f32_32x32x16_bf16 v[48:63], v[76:79], v[146:149], v[48:63]
	v_mfma_f32_32x32x16_bf16 v[48:63], v[80:83], v[150:153], v[48:63]
	v_mfma_f32_32x32x16_bf16 v[48:63], v[84:87], v[154:157], v[48:63]
	s_waitcnt lgkmcnt(0)
	v_mfma_f32_32x32x16_bf16 v[48:63], v[88:91], v[142:145], v[48:63]
	ds_read_b128 v[64:67], v96 offset:32768
	ds_read_b128 v[80:83], v96 offset:40960
	ds_read_b128 v[84:87], v116 offset:32768
	ds_read_b128 v[98:101], v116 offset:40960
	s_waitcnt lgkmcnt(3)
	v_mfma_f32_32x32x16_bf16 v[64:79], v[64:67], v[112:115], 0
	s_waitcnt lgkmcnt(1)
	v_mfma_f32_32x32x16_bf16 v[64:79], v[84:87], v[130:133], v[64:79]
	ds_read_b128 v[84:87], v117 offset:32768
	ds_read_b128 v[102:105], v117 offset:40960
	s_waitcnt lgkmcnt(1)
	v_mfma_f32_32x32x16_bf16 v[64:79], v[84:87], v[134:137], v[64:79]
	ds_read_b128 v[84:87], v118 offset:32768
	ds_read_b128 v[106:109], v118 offset:40960
	s_waitcnt lgkmcnt(1)
	v_mfma_f32_32x32x16_bf16 v[64:79], v[84:87], v[138:141], v[64:79]
	ds_read_b128 v[84:87], v119 offset:32768
	ds_read_b128 v[120:123], v119 offset:40960
	s_waitcnt lgkmcnt(1)
	v_mfma_f32_32x32x16_bf16 v[64:79], v[84:87], v[146:149], v[64:79]
	ds_read_b128 v[84:87], v180 offset:32768
	ds_read_b128 v[124:127], v180 offset:40960
	s_waitcnt lgkmcnt(1)
; #define LAS __attribute__((address_space(3)))
; __device__ __forceinline__ int lane_op() { int l = (int)__builtin_amdgcn_mbcnt_hi(~0u, __builtin_amdgcn_mbcnt_lo(~0u, 0u)); asm volatile("" : "+v"(l)); return l; }
; #define SHX(v, m, l) bperm_((l) ^ (m), (v))
; __device__ __forceinline__ unsigned swap23(unsigned r) { return (r & ~12u) | ((r & 4u) << 1) | ((r & 8u) >> 1); }
; __device__ __forceinline__ void memattn_unit(LAS unsigned char* lds, const bf16* PROJ, const bf16* MKVl, bf16* BR, int b, int hd, int qblk, int tid) {
;     ...
;     for (int kap = 0; kap < 8; ++kap) { f32x16 acc;
; #pragma unroll
;         for (int i = 0; i < 16; ++i) acc[i] = 0.f;
;         const unsigned slot = 32u * kap + swap23((unsigned)r);
; #pragma unroll
;         for (int s = 0; s < 8; ++s) { const bf16x8 a = *(const LAS bf16x8*)(kimg + kv_off(slot, 2 * s + hh)); acc = __builtin_amdgcn_mfma_f32_32x32x16_bf16(a, qf[s], acc, 0, 0, 0); }
;         S[kap] = acc; if (kap & 1) __builtin_amdgcn_sched_barrier(0); }
;     float mx = -INFINITY;
; #pragma unroll
;     for (int kap = 0; kap < 8; ++kap)
; #pragma unroll
;         for (int i = 0; i < 16; ++i) mx = fmaxf(mx, S[kap][i]);
;     const int lop945_ = lane_op(); mx = fmaxf(mx, SHX(mx, 32, lop945_));
	v_mfma_f32_32x32x16_bf16 v[64:79], v[84:87], v[150:153], v[64:79]
	ds_read_b128 v[84:87], v184 offset:32768
	ds_read_b128 v[164:167], v184 offset:40960
	s_waitcnt lgkmcnt(1)
	v_mfma_f32_32x32x16_bf16 v[64:79], v[84:87], v[154:157], v[64:79]
	ds_read_b128 v[84:87], v188 offset:32768
	ds_read_b128 v[168:171], v188 offset:40960
	s_waitcnt lgkmcnt(1)
	v_mfma_f32_32x32x16_bf16 v[64:79], v[84:87], v[142:145], v[64:79]
	v_mfma_f32_32x32x16_bf16 v[80:95], v[80:83], v[112:115], 0
	v_mfma_f32_32x32x16_bf16 v[80:95], v[98:101], v[130:133], v[80:95]
	v_mfma_f32_32x32x16_bf16 v[80:95], v[102:105], v[134:137], v[80:95]
	v_mfma_f32_32x32x16_bf16 v[80:95], v[106:109], v[138:141], v[80:95]
	v_mfma_f32_32x32x16_bf16 v[80:95], v[120:123], v[146:149], v[80:95]
	v_mfma_f32_32x32x16_bf16 v[80:95], v[124:127], v[150:153], v[80:95]
	v_mfma_f32_32x32x16_bf16 v[80:95], v[164:167], v[154:157], v[80:95]
	s_waitcnt lgkmcnt(0)
	v_mfma_f32_32x32x16_bf16 v[80:95], v[168:171], v[142:145], v[80:95]
	ds_read_b128 v[98:101], v96 offset:49152
	ds_read_b128 v[120:123], v96 offset:57344
	ds_read_b128 v[124:127], v116 offset:49152
	ds_read_b128 v[164:167], v116 offset:57344
	s_waitcnt lgkmcnt(3)
	v_mfma_f32_32x32x16_bf16 v[96:111], v[98:101], v[112:115], 0
	s_waitcnt lgkmcnt(1)
	v_mfma_f32_32x32x16_bf16 v[96:111], v[124:127], v[130:133], v[96:111]
	ds_read_b128 v[124:127], v117 offset:49152
	ds_read_b128 v[168:171], v117 offset:57344
	s_waitcnt lgkmcnt(1)
	v_mfma_f32_32x32x16_bf16 v[96:111], v[124:127], v[134:137], v[96:111]
	ds_read_b128 v[124:127], v118 offset:49152
	ds_read_b128 v[172:175], v118 offset:57344
	s_waitcnt lgkmcnt(1)
	v_mfma_f32_32x32x16_bf16 v[96:111], v[124:127], v[138:141], v[96:111]
	ds_read_b128 v[124:127], v119 offset:49152
	ds_read_b128 v[176:179], v119 offset:57344
	ds_read_b128 v[116:119], v180 offset:49152
	ds_read_b128 v[180:183], v180 offset:57344
	s_waitcnt lgkmcnt(3)
	v_mfma_f32_32x32x16_bf16 v[96:111], v[124:127], v[146:149], v[96:111]
	s_waitcnt lgkmcnt(1)
	v_mfma_f32_32x32x16_bf16 v[96:111], v[116:119], v[150:153], v[96:111]
	ds_read_b128 v[116:119], v184 offset:49152
	ds_read_b128 v[184:187], v184 offset:57344
	s_waitcnt lgkmcnt(1)
	v_mfma_f32_32x32x16_bf16 v[96:111], v[116:119], v[154:157], v[96:111]
	ds_read_b128 v[116:119], v188 offset:49152
	ds_read_b128 v[188:191], v188 offset:57344
	s_waitcnt lgkmcnt(1)
	v_mfma_f32_32x32x16_bf16 v[96:111], v[116:119], v[142:145], v[96:111]
	v_mfma_f32_32x32x16_bf16 v[112:127], v[120:123], v[112:115], 0
	v_mfma_f32_32x32x16_bf16 v[112:127], v[164:167], v[130:133], v[112:127]
	v_mfma_f32_32x32x16_bf16 v[112:127], v[168:171], v[134:137], v[112:127]
	v_mfma_f32_32x32x16_bf16 v[112:127], v[172:175], v[138:141], v[112:127]
	v_mfma_f32_32x32x16_bf16 v[112:127], v[176:179], v[146:149], v[112:127]
	v_mfma_f32_32x32x16_bf16 v[112:127], v[180:183], v[150:153], v[112:127]
	v_mfma_f32_32x32x16_bf16 v[112:127], v[184:187], v[154:157], v[112:127]
	s_waitcnt lgkmcnt(0)
	v_mfma_f32_32x32x16_bf16 v[112:127], v[188:191], v[142:145], v[112:127]
	s_mov_b32 s0, 0xff800000
	v_max3_f32 v130, v16, s0, v17
	v_max3_f32 v130, v130, v18, v19
	v_max3_f32 v130, v130, v20, v21
	v_max3_f32 v130, v130, v22, v23
	v_max3_f32 v130, v130, v24, v25
	v_max3_f32 v130, v130, v26, v27
	v_max3_f32 v130, v130, v28, v29
	v_max3_f32 v130, v130, v30, v31
	v_max3_f32 v130, v130, v0, v1
	v_max3_f32 v130, v130, v2, v3
	v_max3_f32 v130, v130, v4, v5
	v_max3_f32 v130, v130, v6, v7
	v_max3_f32 v130, v130, v8, v9
	v_max3_f32 v130, v130, v10, v11
	v_max3_f32 v130, v130, v12, v13
	v_max3_f32 v130, v130, v14, v15
	v_max3_f32 v130, v130, v32, v33
	v_max3_f32 v130, v130, v34, v35
	v_max3_f32 v130, v130, v36, v37
	v_max3_f32 v130, v130, v38, v39
	v_max3_f32 v130, v130, v40, v41
	v_max3_f32 v130, v130, v42, v43
	v_max3_f32 v130, v130, v44, v45
	v_max3_f32 v130, v130, v46, v47
	v_max3_f32 v130, v130, v48, v49
	v_max3_f32 v130, v130, v50, v51
	v_max3_f32 v130, v130, v52, v53
	v_max3_f32 v130, v130, v54, v55
	v_max3_f32 v130, v130, v56, v57
	v_max3_f32 v130, v130, v58, v59
	v_max3_f32 v130, v130, v60, v61
	v_max3_f32 v130, v130, v62, v63
	v_max3_f32 v130, v130, v64, v65
	v_max3_f32 v130, v130, v66, v67
	v_max3_f32 v130, v130, v68, v69
	v_max3_f32 v130, v130, v70, v71
	v_max3_f32 v130, v130, v72, v73
	v_max3_f32 v130, v130, v74, v75
	v_max3_f32 v130, v130, v76, v77
	v_max3_f32 v130, v130, v78, v79
	v_max3_f32 v130, v130, v80, v81
	v_max3_f32 v130, v130, v82, v83
	v_max3_f32 v130, v130, v84, v85
	v_max3_f32 v130, v130, v86, v87
	v_max3_f32 v130, v130, v88, v89
	v_max3_f32 v130, v130, v90, v91
	v_max3_f32 v130, v130, v92, v93
	v_max3_f32 v130, v130, v94, v95
	v_max3_f32 v130, v130, v96, v97
	v_max3_f32 v130, v130, v98, v99
	v_max3_f32 v130, v130, v100, v101
	v_max3_f32 v130, v130, v102, v103
	v_max3_f32 v130, v130, v104, v105
	v_max3_f32 v130, v130, v106, v107
	v_max3_f32 v130, v130, v108, v109
	v_max3_f32 v130, v130, v110, v111
	v_max3_f32 v130, v130, v112, v113
	v_max3_f32 v130, v130, v114, v115
	v_max3_f32 v130, v130, v116, v117
	v_max3_f32 v130, v130, v118, v119
	v_max3_f32 v130, v130, v120, v121
	v_mov_b32_e32 v131, v251
	v_max3_f32 v130, v130, v122, v123
	v_max3_f32 v130, v130, v124, v125
	v_lshlrev_b32_e32 v131, 2, v131
	v_max3_f32 v130, v130, v126, v127
	v_xor_b32_e32 v131, 0x80, v131
	ds_bpermute_b32 v131, v131, v130
	s_waitcnt lgkmcnt(0)
; __device__ __forceinline__ void memattn_unit(LAS unsigned char* lds, const bf16* PROJ, const bf16* MKVl, bf16* BR, int b, int hd, int qblk, int tid) {
;     ...
;     const float sc_ = 0.08838834764831845f * 1.4426950408889634f; float sum = 0.f;
; #pragma unroll
;     for (int kap = 0; kap < 8; ++kap)
; #pragma unroll
;         for (int i = 0; i < 16; ++i) { const float e = __builtin_amdgcn_exp2f((S[kap][i] - mx) * sc_); S[kap][i] = e; sum += e; }
	v_max_f32_e32 v131, v131, v131
	v_max_f32_e32 v131, v130, v131
	v_sub_f32_e32 v16, v16, v131
	v_sub_f32_e32 v17, v17, v131
	v_mul_f32_e32 v16, 0x3e0293ee, v16
	v_mul_f32_e32 v17, 0x3e0293ee, v17
	v_exp_f32_e32 v16, v16
	v_exp_f32_e32 v130, v17
	v_sub_f32_e32 v17, v18, v131
	v_mul_f32_e32 v17, 0x3e0293ee, v17
	v_sub_f32_e32 v18, v19, v131
	v_exp_f32_e32 v17, v17
	v_mul_f32_e32 v18, 0x3e0293ee, v18
	v_exp_f32_e32 v19, v18
	v_add_f32_e32 v18, 0, v16
	v_add_f32_e32 v18, v130, v18
	v_add_f32_e32 v18, v17, v18
	v_add_f32_e32 v135, v19, v18
	v_sub_f32_e32 v18, v20, v131
	v_sub_f32_e32 v20, v21, v131
	v_mul_f32_e32 v20, 0x3e0293ee, v20
	v_mul_f32_e32 v18, 0x3e0293ee, v18
	v_exp_f32_e32 v133, v20
	v_sub_f32_e32 v20, v22, v131
	v_exp_f32_e32 v18, v18
	v_mul_f32_e32 v20, 0x3e0293ee, v20
	v_exp_f32_e32 v132, v20
	v_sub_f32_e32 v20, v23, v131
	v_mul_f32_e32 v20, 0x3e0293ee, v20
	v_exp_f32_e32 v134, v20
	v_add_f32_e32 v20, v18, v135
	v_add_f32_e32 v20, v133, v20
	v_add_f32_e32 v20, v132, v20
	v_add_f32_e32 v23, v134, v20
	v_sub_f32_e32 v20, v24, v131
	v_sub_f32_e32 v21, v25, v131
	v_mul_f32_e32 v20, 0x3e0293ee, v20
	v_mul_f32_e32 v21, 0x3e0293ee, v21
	v_exp_f32_e32 v20, v20
	v_exp_f32_e32 v22, v21
	v_sub_f32_e32 v21, v26, v131
	v_mul_f32_e32 v21, 0x3e0293ee, v21
	v_sub_f32_e32 v24, v27, v131
	v_exp_f32_e32 v21, v21
	v_mul_f32_e32 v24, 0x3e0293ee, v24
	v_exp_f32_e32 v24, v24
	v_add_f32_e32 v23, v20, v23
	v_add_f32_e32 v23, v22, v23
	v_add_f32_e32 v23, v21, v23
	v_add_f32_e32 v135, v24, v23
	v_sub_f32_e32 v23, v28, v131
	v_sub_f32_e32 v25, v29, v131
	v_mul_f32_e32 v23, 0x3e0293ee, v23
	v_mul_f32_e32 v25, 0x3e0293ee, v25
	v_exp_f32_e32 v23, v23
	v_exp_f32_e32 v26, v25
	v_sub_f32_e32 v25, v30, v131
	v_mul_f32_e32 v25, 0x3e0293ee, v25
	v_sub_f32_e32 v27, v31, v131
	v_exp_f32_e32 v25, v25
	v_mul_f32_e32 v27, 0x3e0293ee, v27
	v_exp_f32_e32 v27, v27
	v_sub_f32_e32 v0, v0, v131
	v_add_f32_e32 v28, v23, v135
	v_mul_f32_e32 v0, 0x3e0293ee, v0
	v_add_f32_e32 v28, v26, v28
	v_exp_f32_e32 v0, v0
	v_sub_f32_e32 v1, v1, v131
	v_add_f32_e32 v28, v25, v28
	v_mul_f32_e32 v1, 0x3e0293ee, v1
	v_add_f32_e32 v29, v27, v28
	v_exp_f32_e32 v28, v1
	v_sub_f32_e32 v1, v2, v131
	v_sub_f32_e32 v2, v3, v131
	v_sub_f32_e32 v3, v4, v131
	v_mul_f32_e32 v2, 0x3e0293ee, v2
	v_mul_f32_e32 v3, 0x3e0293ee, v3
	v_mul_f32_e32 v1, 0x3e0293ee, v1
	v_exp_f32_e32 v30, v2
	v_add_f32_e32 v2, v0, v29
	v_exp_f32_e32 v29, v3
	v_sub_f32_e32 v3, v5, v131
	v_exp_f32_e32 v1, v1
	v_mul_f32_e32 v3, 0x3e0293ee, v3
	v_exp_f32_e32 v136, v3
	v_sub_f32_e32 v3, v6, v131
	v_mul_f32_e32 v3, 0x3e0293ee, v3
	v_add_f32_e32 v2, v28, v2
	v_exp_f32_e32 v135, v3
	v_sub_f32_e32 v3, v7, v131
	v_add_f32_e32 v2, v1, v2
	v_mul_f32_e32 v3, 0x3e0293ee, v3
	v_add_f32_e32 v2, v30, v2
	v_exp_f32_e32 v137, v3
	v_add_f32_e32 v2, v29, v2
	v_add_f32_e32 v2, v136, v2
	v_add_f32_e32 v2, v135, v2
	v_sub_f32_e32 v6, v11, v131
	v_add_f32_e32 v4, v137, v2
	v_sub_f32_e32 v2, v8, v131
	v_sub_f32_e32 v3, v9, v131
	v_mul_f32_e32 v6, 0x3e0293ee, v6
	v_mul_f32_e32 v2, 0x3e0293ee, v2
	v_mul_f32_e32 v3, 0x3e0293ee, v3
	v_exp_f32_e32 v9, v6
	v_sub_f32_e32 v6, v12, v131
	v_exp_f32_e32 v2, v2
	v_exp_f32_e32 v5, v3
	v_sub_f32_e32 v3, v10, v131
	v_mul_f32_e32 v6, 0x3e0293ee, v6
	v_mul_f32_e32 v3, 0x3e0293ee, v3
	v_exp_f32_e32 v8, v6
	v_sub_f32_e32 v6, v13, v131
	v_exp_f32_e32 v3, v3
	v_mul_f32_e32 v6, 0x3e0293ee, v6
	v_exp_f32_e32 v138, v6
	v_sub_f32_e32 v6, v14, v131
	v_add_f32_e32 v4, v2, v4
	v_mul_f32_e32 v6, 0x3e0293ee, v6
	v_add_f32_e32 v4, v5, v4
	v_exp_f32_e32 v12, v6
	v_sub_f32_e32 v6, v15, v131
	v_add_f32_e32 v4, v3, v4
	v_mul_f32_e32 v6, 0x3e0293ee, v6
	v_add_f32_e32 v4, v9, v4
	v_exp_f32_e32 v139, v6
	v_add_f32_e32 v4, v8, v4
	v_add_f32_e32 v4, v138, v4
	v_add_f32_e32 v4, v12, v4
	v_sub_f32_e32 v11, v35, v131
	v_add_f32_e32 v7, v139, v4
	v_sub_f32_e32 v4, v32, v131
	v_sub_f32_e32 v6, v33, v131
	v_mul_f32_e32 v11, 0x3e0293ee, v11
	v_mul_f32_e32 v4, 0x3e0293ee, v4
	v_mul_f32_e32 v6, 0x3e0293ee, v6
	v_exp_f32_e32 v15, v11
	v_sub_f32_e32 v11, v36, v131
	v_exp_f32_e32 v4, v4
	v_exp_f32_e32 v10, v6
	v_sub_f32_e32 v6, v34, v131
	v_mul_f32_e32 v11, 0x3e0293ee, v11
	v_mul_f32_e32 v6, 0x3e0293ee, v6
	v_exp_f32_e32 v14, v11
	v_sub_f32_e32 v11, v37, v131
	v_exp_f32_e32 v6, v6
	v_mul_f32_e32 v11, 0x3e0293ee, v11
	v_exp_f32_e32 v33, v11
	v_sub_f32_e32 v11, v38, v131
	v_add_f32_e32 v7, v4, v7
	v_mul_f32_e32 v11, 0x3e0293ee, v11
	v_add_f32_e32 v7, v10, v7
	v_exp_f32_e32 v32, v11
	v_sub_f32_e32 v11, v39, v131
	v_add_f32_e32 v7, v6, v7
	v_mul_f32_e32 v11, 0x3e0293ee, v11
	v_add_f32_e32 v7, v15, v7
	v_exp_f32_e32 v34, v11
	v_add_f32_e32 v7, v14, v7
	v_add_f32_e32 v7, v33, v7
	v_add_f32_e32 v7, v32, v7
	v_sub_f32_e32 v31, v43, v131
	v_add_f32_e32 v13, v34, v7
	v_sub_f32_e32 v7, v40, v131
	v_sub_f32_e32 v11, v41, v131
	v_mul_f32_e32 v31, 0x3e0293ee, v31
	v_mul_f32_e32 v7, 0x3e0293ee, v7
	v_mul_f32_e32 v11, 0x3e0293ee, v11
	v_exp_f32_e32 v38, v31
	v_sub_f32_e32 v31, v44, v131
	v_exp_f32_e32 v7, v7
	v_exp_f32_e32 v36, v11
	v_sub_f32_e32 v11, v42, v131
	v_mul_f32_e32 v31, 0x3e0293ee, v31
	v_mul_f32_e32 v11, 0x3e0293ee, v11
	v_exp_f32_e32 v37, v31
	v_sub_f32_e32 v31, v45, v131
	v_exp_f32_e32 v11, v11
	v_mul_f32_e32 v31, 0x3e0293ee, v31
	v_exp_f32_e32 v140, v31
	v_sub_f32_e32 v31, v46, v131
	v_sub_f32_e32 v35, v49, v131
	v_add_f32_e32 v13, v7, v13
	v_mul_f32_e32 v31, 0x3e0293ee, v31
	v_mul_f32_e32 v35, 0x3e0293ee, v35
	v_add_f32_e32 v13, v36, v13
	v_exp_f32_e32 v39, v31
	v_sub_f32_e32 v31, v47, v131
	v_exp_f32_e32 v46, v35
	v_sub_f32_e32 v35, v50, v131
	v_add_f32_e32 v13, v11, v13
	v_mul_f32_e32 v31, 0x3e0293ee, v31
	v_mul_f32_e32 v35, 0x3e0293ee, v35
; __device__ __forceinline__ void memattn_unit(LAS unsigned char* lds, const bf16* PROJ, const bf16* MKVl, bf16* BR, int b, int hd, int qblk, int tid) {
;     ...
;     const float sc_ = 0.08838834764831845f * 1.4426950408889634f; float sum = 0.f;
; #pragma unroll
;     for (int kap = 0; kap < 8; ++kap)
; #pragma unroll
;         for (int i = 0; i < 16; ++i) { const float e = __builtin_amdgcn_exp2f((S[kap][i] - mx) * sc_); S[kap][i] = e; sum += e; }
	v_add_f32_e32 v13, v38, v13
	v_exp_f32_e32 v142, v31
	v_exp_f32_e32 v44, v35
	v_sub_f32_e32 v35, v51, v131
	v_add_f32_e32 v13, v37, v13
	v_mul_f32_e32 v35, 0x3e0293ee, v35
	v_add_f32_e32 v13, v140, v13
	v_exp_f32_e32 v49, v35
	v_sub_f32_e32 v35, v52, v131
	v_add_f32_e32 v13, v39, v13
	v_mul_f32_e32 v35, 0x3e0293ee, v35
	v_add_f32_e32 v31, v142, v13
	v_sub_f32_e32 v13, v48, v131
	v_exp_f32_e32 v48, v35
	v_sub_f32_e32 v35, v53, v131
	v_mul_f32_e32 v35, 0x3e0293ee, v35
	v_exp_f32_e32 v50, v35
	v_sub_f32_e32 v35, v54, v131
	v_mul_f32_e32 v35, 0x3e0293ee, v35
	v_exp_f32_e32 v51, v35
	v_sub_f32_e32 v35, v55, v131
	v_mul_f32_e32 v35, 0x3e0293ee, v35
	v_exp_f32_e32 v143, v35
	v_sub_f32_e32 v35, v56, v131
	v_mul_f32_e32 v35, 0x3e0293ee, v35
	v_exp_f32_e32 v45, v35
	v_sub_f32_e32 v35, v57, v131
	v_mul_f32_e32 v35, 0x3e0293ee, v35
	v_exp_f32_e32 v141, v35
	v_sub_f32_e32 v35, v58, v131
	v_mul_f32_e32 v35, 0x3e0293ee, v35
	v_exp_f32_e32 v47, v35
	v_sub_f32_e32 v35, v59, v131
	v_mul_f32_e32 v35, 0x3e0293ee, v35
	v_exp_f32_e32 v144, v35
	v_sub_f32_e32 v35, v60, v131
	v_mul_f32_e32 v35, 0x3e0293ee, v35
	v_exp_f32_e32 v145, v35
	v_sub_f32_e32 v35, v61, v131
	v_mul_f32_e32 v35, 0x3e0293ee, v35
	v_exp_f32_e32 v61, v35
	v_sub_f32_e32 v35, v62, v131
	v_mul_f32_e32 v35, 0x3e0293ee, v35
	v_exp_f32_e32 v62, v35
	v_sub_f32_e32 v35, v63, v131
	v_mul_f32_e32 v35, 0x3e0293ee, v35
	v_exp_f32_e32 v63, v35
	v_sub_f32_e32 v35, v64, v131
	v_mul_f32_e32 v35, 0x3e0293ee, v35
	v_exp_f32_e32 v60, v35
	v_sub_f32_e32 v35, v65, v131
	v_mul_f32_e32 v35, 0x3e0293ee, v35
	v_exp_f32_e32 v146, v35
	v_sub_f32_e32 v35, v66, v131
	v_mul_f32_e32 v35, 0x3e0293ee, v35
	v_exp_f32_e32 v147, v35
	v_sub_f32_e32 v35, v67, v131
	v_mul_f32_e32 v35, 0x3e0293ee, v35
	v_exp_f32_e32 v148, v35
	v_sub_f32_e32 v35, v68, v131
	v_mul_f32_e32 v35, 0x3e0293ee, v35
	v_exp_f32_e32 v68, v35
	v_sub_f32_e32 v35, v69, v131
	v_mul_f32_e32 v35, 0x3e0293ee, v35
	v_exp_f32_e32 v69, v35
	v_sub_f32_e32 v35, v70, v131
	v_mul_f32_e32 v35, 0x3e0293ee, v35
	v_exp_f32_e32 v70, v35
	v_sub_f32_e32 v35, v71, v131
	v_mul_f32_e32 v35, 0x3e0293ee, v35
	v_exp_f32_e32 v71, v35
	v_sub_f32_e32 v35, v72, v131
	v_mul_f32_e32 v35, 0x3e0293ee, v35
	v_exp_f32_e32 v72, v35
	v_sub_f32_e32 v35, v73, v131
	v_mul_f32_e32 v35, 0x3e0293ee, v35
	v_exp_f32_e32 v73, v35
	v_sub_f32_e32 v35, v74, v131
	v_mul_f32_e32 v35, 0x3e0293ee, v35
	v_exp_f32_e32 v74, v35
	v_sub_f32_e32 v35, v75, v131
	v_mul_f32_e32 v35, 0x3e0293ee, v35
	v_exp_f32_e32 v75, v35
	v_sub_f32_e32 v35, v76, v131
	v_mul_f32_e32 v35, 0x3e0293ee, v35
	v_exp_f32_e32 v76, v35
	v_sub_f32_e32 v35, v77, v131
	v_mul_f32_e32 v35, 0x3e0293ee, v35
	v_exp_f32_e32 v77, v35
	v_sub_f32_e32 v35, v78, v131
	v_mul_f32_e32 v35, 0x3e0293ee, v35
	v_exp_f32_e32 v78, v35
	v_sub_f32_e32 v35, v79, v131
	v_mul_f32_e32 v35, 0x3e0293ee, v35
	v_exp_f32_e32 v79, v35
	v_sub_f32_e32 v35, v80, v131
	v_mul_f32_e32 v35, 0x3e0293ee, v35
	v_exp_f32_e32 v80, v35
	v_sub_f32_e32 v35, v81, v131
	v_mul_f32_e32 v35, 0x3e0293ee, v35
	v_exp_f32_e32 v81, v35
	v_sub_f32_e32 v35, v82, v131
	v_mul_f32_e32 v35, 0x3e0293ee, v35
	v_exp_f32_e32 v82, v35
	v_sub_f32_e32 v35, v83, v131
	v_mul_f32_e32 v35, 0x3e0293ee, v35
	v_exp_f32_e32 v83, v35
	v_sub_f32_e32 v35, v84, v131
	v_mul_f32_e32 v35, 0x3e0293ee, v35
	v_exp_f32_e32 v84, v35
	v_sub_f32_e32 v35, v85, v131
	v_mul_f32_e32 v35, 0x3e0293ee, v35
	v_exp_f32_e32 v85, v35
	v_sub_f32_e32 v35, v86, v131
	v_mul_f32_e32 v35, 0x3e0293ee, v35
	v_exp_f32_e32 v86, v35
	v_sub_f32_e32 v35, v87, v131
	v_mul_f32_e32 v35, 0x3e0293ee, v35
	v_mul_f32_e32 v13, 0x3e0293ee, v13
	v_exp_f32_e32 v87, v35
	v_sub_f32_e32 v35, v88, v131
	v_exp_f32_e32 v13, v13
	v_mul_f32_e32 v35, 0x3e0293ee, v35
	v_exp_f32_e32 v88, v35
	v_sub_f32_e32 v35, v89, v131
	v_mul_f32_e32 v35, 0x3e0293ee, v35
	v_exp_f32_e32 v89, v35
	v_sub_f32_e32 v35, v90, v131
	v_add_f32_e32 v31, v13, v31
	v_mul_f32_e32 v35, 0x3e0293ee, v35
	v_add_f32_e32 v31, v46, v31
	v_exp_f32_e32 v90, v35
	v_sub_f32_e32 v35, v91, v131
	v_add_f32_e32 v31, v44, v31
	v_mul_f32_e32 v35, 0x3e0293ee, v35
	v_add_f32_e32 v31, v49, v31
	v_exp_f32_e32 v91, v35
	v_sub_f32_e32 v35, v92, v131
	v_add_f32_e32 v31, v48, v31
	v_mul_f32_e32 v35, 0x3e0293ee, v35
	v_add_f32_e32 v31, v50, v31
	v_exp_f32_e32 v92, v35
	v_sub_f32_e32 v35, v93, v131
	v_add_f32_e32 v31, v51, v31
	v_mul_f32_e32 v35, 0x3e0293ee, v35
	v_add_f32_e32 v31, v143, v31
	v_exp_f32_e32 v93, v35
	v_sub_f32_e32 v35, v94, v131
	v_add_f32_e32 v31, v45, v31
	v_mul_f32_e32 v35, 0x3e0293ee, v35
	v_add_f32_e32 v31, v141, v31
	v_exp_f32_e32 v94, v35
	v_sub_f32_e32 v35, v95, v131
	v_add_f32_e32 v31, v47, v31
	v_mul_f32_e32 v35, 0x3e0293ee, v35
	v_add_f32_e32 v31, v144, v31
	v_exp_f32_e32 v95, v35
	v_sub_f32_e32 v35, v96, v131
	v_add_f32_e32 v31, v145, v31
	v_mul_f32_e32 v35, 0x3e0293ee, v35
	v_add_f32_e32 v31, v61, v31
	v_exp_f32_e32 v96, v35
	v_sub_f32_e32 v35, v97, v131
	v_add_f32_e32 v31, v62, v31
	v_mul_f32_e32 v35, 0x3e0293ee, v35
	v_add_f32_e32 v31, v63, v31
	v_exp_f32_e32 v97, v35
	v_sub_f32_e32 v35, v98, v131
	v_add_f32_e32 v31, v60, v31
	v_mul_f32_e32 v35, 0x3e0293ee, v35
	v_add_f32_e32 v31, v146, v31
	v_exp_f32_e32 v98, v35
	v_sub_f32_e32 v35, v99, v131
	v_add_f32_e32 v31, v147, v31
	v_mul_f32_e32 v35, 0x3e0293ee, v35
	v_add_f32_e32 v31, v148, v31
	v_exp_f32_e32 v99, v35
	v_sub_f32_e32 v35, v100, v131
	v_add_f32_e32 v31, v68, v31
	v_mul_f32_e32 v35, 0x3e0293ee, v35
	v_add_f32_e32 v31, v69, v31
	v_exp_f32_e32 v100, v35
	v_sub_f32_e32 v35, v101, v131
	v_add_f32_e32 v31, v70, v31
	v_mul_f32_e32 v35, 0x3e0293ee, v35
	v_add_f32_e32 v31, v71, v31
	v_exp_f32_e32 v101, v35
	v_sub_f32_e32 v35, v102, v131
	v_add_f32_e32 v31, v72, v31
; __device__ __forceinline__ unsigned pk2(float lo, float hi) { return f2bf(lo) | (f2bf(hi) << 16); }
; __device__ __forceinline__ int lane_op() { int l = (int)__builtin_amdgcn_mbcnt_hi(~0u, __builtin_amdgcn_mbcnt_lo(~0u, 0u)); asm volatile("" : "+v"(l)); return l; }
; #define SHX(v, m, l) bperm_((l) ^ (m), (v))
; __device__ __forceinline__ void memattn_unit(LAS unsigned char* lds, const bf16* PROJ, const bf16* MKVl, bf16* BR, int b, int hd, int qblk, int tid) {
;     ...
;         for (int i = 0; i < 16; ++i) { const float e = __builtin_amdgcn_exp2f((S[kap][i] - mx) * sc_); S[kap][i] = e; sum += e; }
;     const int lop951_ = lane_op(); sum += SHX(sum, 32, lop951_);
;     const float inv = 1.f / sum;
;     bf16x8 Bp[16];
; #pragma unroll
;     for (int kap = 0; kap < 8; ++kap)
; #pragma unroll
;         for (int s = 0; s < 2; ++s) { v4u w; w.x = pk2(S[kap][8 * s], S[kap][8 * s + 1]); w.y = pk2(S[kap][8 * s + 2], S[kap][8 * s + 3]); w.z = pk2(S[kap][8 * s + 4], S[kap][8 * s + 5]); w.w = pk2(S[kap][8 * s + 6], S[kap][8 * s + 7]);
	v_mul_f32_e32 v35, 0x3e0293ee, v35
	v_add_f32_e32 v31, v73, v31
	v_exp_f32_e32 v102, v35
	v_sub_f32_e32 v35, v103, v131
	v_add_f32_e32 v31, v74, v31
	v_mul_f32_e32 v35, 0x3e0293ee, v35
	v_add_f32_e32 v31, v75, v31
	v_exp_f32_e32 v103, v35
	v_sub_f32_e32 v35, v104, v131
	v_add_f32_e32 v31, v76, v31
	v_mul_f32_e32 v35, 0x3e0293ee, v35
	v_add_f32_e32 v31, v77, v31
	v_exp_f32_e32 v104, v35
	v_sub_f32_e32 v35, v105, v131
	v_add_f32_e32 v31, v78, v31
	v_mul_f32_e32 v35, 0x3e0293ee, v35
	v_add_f32_e32 v31, v79, v31
	v_exp_f32_e32 v105, v35
	v_sub_f32_e32 v35, v106, v131
	v_add_f32_e32 v31, v80, v31
	v_mul_f32_e32 v35, 0x3e0293ee, v35
	v_add_f32_e32 v31, v81, v31
	v_exp_f32_e32 v106, v35
	v_sub_f32_e32 v35, v107, v131
	v_add_f32_e32 v31, v82, v31
	v_mul_f32_e32 v35, 0x3e0293ee, v35
	v_add_f32_e32 v31, v83, v31
	v_exp_f32_e32 v107, v35
	v_sub_f32_e32 v35, v108, v131
	v_add_f32_e32 v31, v84, v31
	v_mul_f32_e32 v35, 0x3e0293ee, v35
	v_add_f32_e32 v31, v85, v31
	v_exp_f32_e32 v108, v35
	v_sub_f32_e32 v35, v109, v131
	v_add_f32_e32 v31, v86, v31
	v_mul_f32_e32 v35, 0x3e0293ee, v35
	v_add_f32_e32 v31, v87, v31
	v_exp_f32_e32 v109, v35
	v_sub_f32_e32 v35, v110, v131
	v_add_f32_e32 v31, v88, v31
	v_mul_f32_e32 v35, 0x3e0293ee, v35
	v_add_f32_e32 v31, v89, v31
	v_exp_f32_e32 v110, v35
	v_sub_f32_e32 v35, v111, v131
	v_add_f32_e32 v31, v90, v31
	v_mul_f32_e32 v35, 0x3e0293ee, v35
	v_add_f32_e32 v31, v91, v31
	v_exp_f32_e32 v111, v35
	v_sub_f32_e32 v35, v112, v131
	v_add_f32_e32 v31, v92, v31
	v_mul_f32_e32 v35, 0x3e0293ee, v35
	v_add_f32_e32 v31, v93, v31
	v_exp_f32_e32 v112, v35
	v_sub_f32_e32 v35, v113, v131
	v_add_f32_e32 v31, v94, v31
	v_mul_f32_e32 v35, 0x3e0293ee, v35
	v_add_f32_e32 v31, v95, v31
	v_exp_f32_e32 v113, v35
	v_sub_f32_e32 v35, v114, v131
	v_add_f32_e32 v31, v96, v31
	v_mul_f32_e32 v35, 0x3e0293ee, v35
	v_add_f32_e32 v31, v97, v31
	v_exp_f32_e32 v114, v35
	v_sub_f32_e32 v35, v115, v131
	v_add_f32_e32 v31, v98, v31
	v_mul_f32_e32 v35, 0x3e0293ee, v35
	v_add_f32_e32 v31, v99, v31
	v_exp_f32_e32 v115, v35
	v_sub_f32_e32 v35, v116, v131
	v_add_f32_e32 v31, v100, v31
	v_mul_f32_e32 v35, 0x3e0293ee, v35
	v_add_f32_e32 v31, v101, v31
	v_exp_f32_e32 v116, v35
	v_sub_f32_e32 v35, v117, v131
	v_add_f32_e32 v31, v102, v31
	v_mul_f32_e32 v35, 0x3e0293ee, v35
	v_add_f32_e32 v31, v103, v31
	v_exp_f32_e32 v117, v35
	v_sub_f32_e32 v35, v118, v131
	v_add_f32_e32 v31, v104, v31
	v_mul_f32_e32 v35, 0x3e0293ee, v35
	v_add_f32_e32 v31, v105, v31
	v_exp_f32_e32 v118, v35
	v_sub_f32_e32 v35, v119, v131
	v_add_f32_e32 v31, v106, v31
	v_mul_f32_e32 v35, 0x3e0293ee, v35
	v_add_f32_e32 v31, v107, v31
	v_exp_f32_e32 v119, v35
	v_sub_f32_e32 v35, v120, v131
	v_add_f32_e32 v31, v108, v31
	v_mul_f32_e32 v35, 0x3e0293ee, v35
	v_add_f32_e32 v31, v109, v31
	v_exp_f32_e32 v120, v35
	v_sub_f32_e32 v35, v121, v131
	v_add_f32_e32 v31, v110, v31
	v_mul_f32_e32 v35, 0x3e0293ee, v35
	v_add_f32_e32 v31, v111, v31
	v_exp_f32_e32 v121, v35
	v_sub_f32_e32 v35, v122, v131
	v_add_f32_e32 v31, v112, v31
	v_mul_f32_e32 v35, 0x3e0293ee, v35
	v_add_f32_e32 v31, v113, v31
	v_exp_f32_e32 v122, v35
	v_sub_f32_e32 v35, v123, v131
	v_add_f32_e32 v31, v114, v31
	v_mul_f32_e32 v35, 0x3e0293ee, v35
	v_add_f32_e32 v31, v115, v31
	v_exp_f32_e32 v123, v35
	v_sub_f32_e32 v35, v124, v131
	v_add_f32_e32 v31, v116, v31
	v_mul_f32_e32 v35, 0x3e0293ee, v35
	v_add_f32_e32 v31, v117, v31
	v_exp_f32_e32 v124, v35
	v_sub_f32_e32 v35, v125, v131
	v_add_f32_e32 v31, v118, v31
	v_mul_f32_e32 v35, 0x3e0293ee, v35
	v_add_f32_e32 v31, v119, v31
	v_exp_f32_e32 v125, v35
	v_sub_f32_e32 v35, v126, v131
	v_add_f32_e32 v31, v120, v31
	v_mul_f32_e32 v35, 0x3e0293ee, v35
	v_add_f32_e32 v31, v121, v31
	v_exp_f32_e32 v126, v35
	v_sub_f32_e32 v35, v127, v131
	v_add_f32_e32 v31, v122, v31
	v_mul_f32_e32 v35, 0x3e0293ee, v35
	v_add_f32_e32 v31, v123, v31
	v_exp_f32_e32 v127, v35
	v_add_f32_e32 v31, v124, v31
	v_mov_b32_e32 v35, v251
	v_add_f32_e32 v31, v125, v31
	v_add_f32_e32 v31, v126, v31
	v_lshlrev_b32_e32 v35, 2, v35
	v_add_f32_e32 v31, v127, v31
	v_xor_b32_e32 v35, 0x80, v35
	ds_bpermute_b32 v35, v35, v31
	v_bfe_u32 v41, v19, 16, 1
	v_bfe_u32 v43, v17, 16, 1
	v_bfe_u32 v52, v18, 16, 1
	v_bfe_u32 v53, v132, 16, 1
	s_waitcnt lgkmcnt(0)
; __device__ __forceinline__ unsigned pk2(float lo, float hi) { return f2bf(lo) | (f2bf(hi) << 16); }
; __device__ __forceinline__ int lane_op() { int l = (int)__builtin_amdgcn_mbcnt_hi(~0u, __builtin_amdgcn_mbcnt_lo(~0u, 0u)); asm volatile("" : "+v"(l)); return l; }
; #define SHX(v, m, l) bperm_((l) ^ (m), (v))
; __device__ __forceinline__ void memattn_unit(LAS unsigned char* lds, const bf16* PROJ, const bf16* MKVl, bf16* BR, int b, int hd, int qblk, int tid) {
;     ...
;     const int lop951_ = lane_op(); sum += SHX(sum, 32, lop951_);
;     const float inv = 1.f / sum;
;     bf16x8 Bp[16];
; #pragma unroll
;     for (int kap = 0; kap < 8; ++kap)
; #pragma unroll
;         for (int s = 0; s < 2; ++s) { v4u w; w.x = pk2(S[kap][8 * s], S[kap][8 * s + 1]); w.y = pk2(S[kap][8 * s + 2], S[kap][8 * s + 3]); w.z = pk2(S[kap][8 * s + 4], S[kap][8 * s + 5]); w.w = pk2(S[kap][8 * s + 6], S[kap][8 * s + 7]);
;             Bp[2 * kap + s] = __builtin_bit_cast(bf16x8, w); }
	v_add_f32_e32 v31, v31, v35
	v_bfe_u32 v35, v134, 16, 1
	v_bfe_u32 v40, v133, 16, 1
	v_add3_u32 v19, v19, v41, s55
	v_bfe_u32 v41, v16, 16, 1
	v_add3_u32 v53, v132, v53, s55
	v_add3_u32 v18, v18, v52, s55
	v_add3_u32 v17, v17, v43, s55
	v_bfe_u32 v42, v130, 16, 1
	v_add3_u32 v40, v133, v40, s55
	v_add3_u32 v35, v134, v35, s55
	v_add3_u32 v16, v16, v41, s55
	v_lshrrev_b32_e32 v17, 16, v17
	v_lshrrev_b32_e32 v18, 16, v18
	v_lshrrev_b32_e32 v41, 16, v53
	v_add3_u32 v42, v130, v42, s55
	v_lshrrev_b32_e32 v16, 16, v16
	v_and_or_b32 v55, v35, s53, v41
	v_and_or_b32 v54, v40, s53, v18
	v_and_or_b32 v53, v19, s53, v17
	v_bfe_u32 v19, v28, 16, 1
	v_bfe_u32 v35, v29, 16, 1
	v_bfe_u32 v40, v135, 16, 1
	v_and_or_b32 v52, v42, s53, v16
	v_bfe_u32 v16, v137, 16, 1
	v_bfe_u32 v17, v136, 16, 1
	v_bfe_u32 v18, v30, 16, 1
	v_add3_u32 v19, v28, v19, s55
	v_bfe_u32 v28, v0, 16, 1
	v_add3_u32 v40, v135, v40, s55
	v_add3_u32 v29, v29, v35, s55
	v_add3_u32 v18, v30, v18, s55
	v_add3_u32 v17, v136, v17, s55
	v_add3_u32 v16, v137, v16, s55
	v_bfe_u32 v30, v1, 16, 1
	v_add3_u32 v0, v0, v28, s55
	v_lshrrev_b32_e32 v28, 16, v29
	v_lshrrev_b32_e32 v29, 16, v40
	v_add3_u32 v1, v1, v30, s55
	v_and_or_b32 v59, v16, s53, v29
	v_and_or_b32 v58, v17, s53, v28
	v_bfe_u32 v16, v9, 16, 1
	v_bfe_u32 v17, v5, 16, 1
	v_lshrrev_b32_e32 v1, 16, v1
	v_add3_u32 v5, v5, v17, s55
	v_add3_u32 v9, v9, v16, s55
	v_bfe_u32 v16, v2, 16, 1
	v_bfe_u32 v17, v3, 16, 1
	v_lshrrev_b32_e32 v0, 16, v0
	v_and_or_b32 v57, v18, s53, v1
	v_bfe_u32 v18, v8, 16, 1
	v_add3_u32 v3, v3, v17, s55
	v_add3_u32 v2, v2, v16, s55
	v_and_or_b32 v56, v19, s53, v0
	v_bfe_u32 v1, v138, 16, 1
	v_bfe_u32 v19, v12, 16, 1
	v_add3_u32 v8, v8, v18, s55
	v_lshrrev_b32_e32 v2, 16, v2
	v_lshrrev_b32_e32 v3, 16, v3
	v_bfe_u32 v0, v139, 16, 1
	v_add3_u32 v1, v138, v1, s55
	v_add3_u32 v12, v12, v19, s55
	v_lshrrev_b32_e32 v8, 16, v8
	v_and_or_b32 v41, v9, s53, v3
	v_and_or_b32 v40, v5, s53, v2
	v_bfe_u32 v3, v10, 16, 1
	v_bfe_u32 v5, v4, 16, 1
	v_add3_u32 v0, v139, v0, s55
	v_lshrrev_b32_e32 v12, 16, v12
	v_and_or_b32 v42, v1, s53, v8
	v_add3_u32 v3, v10, v3, s55
	v_bfe_u32 v8, v6, 16, 1
	v_bfe_u32 v9, v14, 16, 1
	v_bfe_u32 v10, v32, 16, 1
	v_add3_u32 v4, v4, v5, s55
	v_and_or_b32 v43, v0, s53, v12
	v_bfe_u32 v0, v34, 16, 1
	v_bfe_u32 v1, v33, 16, 1
	v_bfe_u32 v2, v15, 16, 1
	v_add3_u32 v10, v32, v10, s55
	v_add3_u32 v9, v14, v9, s55
	v_add3_u32 v6, v6, v8, s55
	v_lshrrev_b32_e32 v4, 16, v4
	v_add3_u32 v2, v15, v2, s55
	v_add3_u32 v1, v33, v1, s55
	v_add3_u32 v0, v34, v0, s55
	v_lshrrev_b32_e32 v5, 16, v6
	v_lshrrev_b32_e32 v6, 16, v9
	v_lshrrev_b32_e32 v8, 16, v10
	v_and_or_b32 v32, v3, s53, v4
	v_bfe_u32 v4, v7, 16, 1
	v_and_or_b32 v35, v0, s53, v8
	v_and_or_b32 v34, v1, s53, v6
	v_and_or_b32 v33, v2, s53, v5
	v_bfe_u32 v3, v36, 16, 1
	v_bfe_u32 v5, v11, 16, 1
	v_bfe_u32 v6, v37, 16, 1
	v_bfe_u32 v8, v39, 16, 1
	v_add3_u32 v4, v7, v4, s55
	v_bfe_u32 v0, v142, 16, 1
	v_bfe_u32 v1, v140, 16, 1
	v_bfe_u32 v2, v38, 16, 1
	v_add3_u32 v3, v36, v3, s55
	v_add3_u32 v8, v39, v8, s55
	v_add3_u32 v6, v37, v6, s55
	v_add3_u32 v5, v11, v5, s55
	v_lshrrev_b32_e32 v4, 16, v4
	v_add3_u32 v2, v38, v2, s55
	v_add3_u32 v1, v140, v1, s55
	v_add3_u32 v0, v142, v0, s55
	v_lshrrev_b32_e32 v5, 16, v5
	v_lshrrev_b32_e32 v6, 16, v6
	v_lshrrev_b32_e32 v7, 16, v8
	v_and_or_b32 v36, v3, s53, v4
	v_bfe_u32 v4, v13, 16, 1
	v_and_or_b32 v39, v0, s53, v7
	v_and_or_b32 v38, v1, s53, v6
	v_and_or_b32 v37, v2, s53, v5
	v_bfe_u32 v3, v46, 16, 1
	v_bfe_u32 v5, v44, 16, 1
	v_bfe_u32 v6, v48, 16, 1
	v_bfe_u32 v7, v51, 16, 1
	v_add3_u32 v4, v13, v4, s55
	v_bfe_u32 v0, v143, 16, 1
	v_bfe_u32 v1, v50, 16, 1
	v_bfe_u32 v2, v49, 16, 1
	v_add3_u32 v3, v46, v3, s55
	v_add3_u32 v7, v51, v7, s55
	v_add3_u32 v6, v48, v6, s55
	v_add3_u32 v5, v44, v5, s55
	v_lshrrev_b32_e32 v4, 16, v4
	v_add3_u32 v2, v49, v2, s55
	v_add3_u32 v1, v50, v1, s55
	v_add3_u32 v0, v143, v0, s55
	v_lshrrev_b32_e32 v5, 16, v5
	v_lshrrev_b32_e32 v6, 16, v6
	v_lshrrev_b32_e32 v7, 16, v7
	v_and_or_b32 v48, v3, s53, v4
	v_bfe_u32 v4, v45, 16, 1
	v_and_or_b32 v51, v0, s53, v7
	v_and_or_b32 v50, v1, s53, v6
	v_and_or_b32 v49, v2, s53, v5
	v_bfe_u32 v3, v141, 16, 1
	v_bfe_u32 v5, v47, 16, 1
	v_bfe_u32 v6, v145, 16, 1
	v_bfe_u32 v7, v62, 16, 1
	v_add3_u32 v4, v45, v4, s55
	v_bfe_u32 v0, v63, 16, 1
	v_bfe_u32 v1, v61, 16, 1
	v_bfe_u32 v2, v144, 16, 1
	v_add3_u32 v3, v141, v3, s55
	v_add3_u32 v7, v62, v7, s55
	v_add3_u32 v6, v145, v6, s55
	v_add3_u32 v5, v47, v5, s55
	v_lshrrev_b32_e32 v4, 16, v4
	v_add3_u32 v2, v144, v2, s55
	v_add3_u32 v1, v61, v1, s55
	v_add3_u32 v0, v63, v0, s55
	v_lshrrev_b32_e32 v5, 16, v5
	v_lshrrev_b32_e32 v6, 16, v6
	v_lshrrev_b32_e32 v7, 16, v7
	v_and_or_b32 v64, v3, s53, v4
	v_bfe_u32 v4, v60, 16, 1
	v_and_or_b32 v67, v0, s53, v7
	v_and_or_b32 v66, v1, s53, v6
	v_and_or_b32 v65, v2, s53, v5
	v_bfe_u32 v3, v146, 16, 1
	v_bfe_u32 v5, v147, 16, 1
	v_bfe_u32 v6, v68, 16, 1
	v_bfe_u32 v7, v70, 16, 1
	v_add3_u32 v4, v60, v4, s55
	v_bfe_u32 v0, v71, 16, 1
	v_bfe_u32 v1, v69, 16, 1
	v_bfe_u32 v2, v148, 16, 1
	v_add3_u32 v3, v146, v3, s55
	v_add3_u32 v7, v70, v7, s55
	v_add3_u32 v6, v68, v6, s55
	v_add3_u32 v5, v147, v5, s55
	v_lshrrev_b32_e32 v4, 16, v4
	v_add3_u32 v2, v148, v2, s55
	v_add3_u32 v1, v69, v1, s55
	v_add3_u32 v0, v71, v0, s55
	v_lshrrev_b32_e32 v5, 16, v5
	v_lshrrev_b32_e32 v6, 16, v6
	v_lshrrev_b32_e32 v7, 16, v7
	v_and_or_b32 v44, v3, s53, v4
	v_bfe_u32 v4, v72, 16, 1
	v_and_or_b32 v47, v0, s53, v7
	v_and_or_b32 v46, v1, s53, v6
	v_and_or_b32 v45, v2, s53, v5
	v_bfe_u32 v3, v73, 16, 1
	v_bfe_u32 v5, v74, 16, 1
	v_bfe_u32 v6, v76, 16, 1
	v_bfe_u32 v7, v78, 16, 1
; #define LAS __attribute__((address_space(3)))
; __device__ __forceinline__ unsigned pk2(float lo, float hi) { return f2bf(lo) | (f2bf(hi) << 16); }
; __device__ __forceinline__ void memattn_unit(LAS unsigned char* lds, const bf16* PROJ, const bf16* MKVl, bf16* BR, int b, int hd, int qblk, int tid) {
;     ...
;         for (int s = 0; s < 2; ++s) { v4u w; w.x = pk2(S[kap][8 * s], S[kap][8 * s + 1]); w.y = pk2(S[kap][8 * s + 2], S[kap][8 * s + 3]); w.z = pk2(S[kap][8 * s + 4], S[kap][8 * s + 5]); w.w = pk2(S[kap][8 * s + 6], S[kap][8 * s + 7]);
;             Bp[2 * kap + s] = __builtin_bit_cast(bf16x8, w); }
;     const unsigned blk = (lane >> 4) & 1, q4 = (lane & 15) >> 2, p = lane & 3;
;     bf16* orow = BR + tok * 2048 + 1536 + hd * 128;
; #pragma unroll
;     for (int c = 0; c < 4; ++c) { f32x16 o;
; #pragma unroll
;         for (int i = 0; i < 16; ++i) o[i] = 0.f;
; #pragma unroll
;         for (int ks = 0; ks < 16; ++ks) {
;             const v4i16_t lo = __builtin_amdgcn_ds_read_tr16_b64_v4i16((LAS v4i16_t*)(vimg + kv_off(16u * ks + 8u * hh + q4, 4u * c + 2u * blk + (p >> 1)) + 8u * (p & 1u)));
;             const v4i16_t hi = __builtin_amdgcn_ds_read_tr16_b64_v4i16((LAS v4i16_t*)(vimg + kv_off(16u * ks + 8u * hh + 4u + q4, 4u * c + 2u * blk + (p >> 1)) + 8u * (p & 1u)));
;             const bf16x8 a = __builtin_shufflevector(lo, hi, 0, 1, 2, 3, 4, 5, 6, 7);
	v_add3_u32 v4, v72, v4, s55
	v_bfe_u32 v0, v79, 16, 1
	v_bfe_u32 v1, v77, 16, 1
	v_bfe_u32 v2, v75, 16, 1
	v_add3_u32 v3, v73, v3, s55
	v_add3_u32 v7, v78, v7, s55
	v_add3_u32 v6, v76, v6, s55
	v_add3_u32 v5, v74, v5, s55
	v_lshrrev_b32_e32 v4, 16, v4
	v_add3_u32 v2, v75, v2, s55
	v_add3_u32 v1, v77, v1, s55
	v_add3_u32 v0, v79, v0, s55
	v_lshrrev_b32_e32 v5, 16, v5
	v_lshrrev_b32_e32 v6, 16, v6
	v_lshrrev_b32_e32 v7, 16, v7
	v_and_or_b32 v60, v3, s53, v4
	v_bfe_u32 v4, v80, 16, 1
	v_and_or_b32 v63, v0, s53, v7
	v_and_or_b32 v62, v1, s53, v6
	v_and_or_b32 v61, v2, s53, v5
	v_bfe_u32 v3, v81, 16, 1
	v_bfe_u32 v5, v82, 16, 1
	v_bfe_u32 v6, v84, 16, 1
	v_bfe_u32 v7, v86, 16, 1
	v_add3_u32 v4, v80, v4, s55
	v_bfe_u32 v0, v87, 16, 1
	v_bfe_u32 v1, v85, 16, 1
	v_bfe_u32 v2, v83, 16, 1
	v_add3_u32 v3, v81, v3, s55
	v_add3_u32 v7, v86, v7, s55
	v_add3_u32 v6, v84, v6, s55
	v_add3_u32 v5, v82, v5, s55
	v_lshrrev_b32_e32 v4, 16, v4
	v_add3_u32 v2, v83, v2, s55
	v_add3_u32 v1, v85, v1, s55
	v_add3_u32 v0, v87, v0, s55
	v_lshrrev_b32_e32 v5, 16, v5
	v_lshrrev_b32_e32 v6, 16, v6
	v_lshrrev_b32_e32 v7, 16, v7
	v_and_or_b32 v72, v3, s53, v4
	v_bfe_u32 v4, v88, 16, 1
	v_and_or_b32 v75, v0, s53, v7
	v_and_or_b32 v74, v1, s53, v6
	v_and_or_b32 v73, v2, s53, v5
	v_bfe_u32 v3, v89, 16, 1
	v_bfe_u32 v5, v90, 16, 1
	v_bfe_u32 v6, v92, 16, 1
	v_bfe_u32 v7, v94, 16, 1
	v_add3_u32 v4, v88, v4, s55
	v_bfe_u32 v0, v95, 16, 1
	v_bfe_u32 v1, v93, 16, 1
	v_bfe_u32 v2, v91, 16, 1
	v_add3_u32 v3, v89, v3, s55
	v_add3_u32 v7, v94, v7, s55
	v_add3_u32 v6, v92, v6, s55
	v_add3_u32 v5, v90, v5, s55
	v_lshrrev_b32_e32 v4, 16, v4
	v_add3_u32 v2, v91, v2, s55
	v_add3_u32 v1, v93, v1, s55
	v_add3_u32 v0, v95, v0, s55
	v_lshrrev_b32_e32 v5, 16, v5
	v_lshrrev_b32_e32 v6, 16, v6
	v_lshrrev_b32_e32 v7, 16, v7
	v_and_or_b32 v80, v3, s53, v4
	v_bfe_u32 v4, v96, 16, 1
	v_and_or_b32 v83, v0, s53, v7
	v_and_or_b32 v82, v1, s53, v6
	v_and_or_b32 v81, v2, s53, v5
	v_bfe_u32 v3, v97, 16, 1
	v_bfe_u32 v5, v98, 16, 1
	v_bfe_u32 v6, v100, 16, 1
	v_bfe_u32 v7, v102, 16, 1
	v_add3_u32 v4, v96, v4, s55
	v_bfe_u32 v0, v103, 16, 1
	v_bfe_u32 v1, v101, 16, 1
	v_bfe_u32 v2, v99, 16, 1
	v_add3_u32 v3, v97, v3, s55
	v_add3_u32 v7, v102, v7, s55
	v_add3_u32 v6, v100, v6, s55
	v_add3_u32 v5, v98, v5, s55
	v_lshrrev_b32_e32 v4, 16, v4
	v_add3_u32 v2, v99, v2, s55
	v_add3_u32 v1, v101, v1, s55
	v_add3_u32 v0, v103, v0, s55
	v_lshrrev_b32_e32 v5, 16, v5
	v_lshrrev_b32_e32 v6, 16, v6
	v_lshrrev_b32_e32 v7, 16, v7
	v_and_or_b32 v68, v3, s53, v4
	v_bfe_u32 v4, v104, 16, 1
	v_and_or_b32 v71, v0, s53, v7
	v_and_or_b32 v70, v1, s53, v6
	v_and_or_b32 v69, v2, s53, v5
	v_bfe_u32 v3, v105, 16, 1
	v_bfe_u32 v5, v106, 16, 1
	v_bfe_u32 v6, v108, 16, 1
	v_bfe_u32 v7, v110, 16, 1
	v_add3_u32 v4, v104, v4, s55
	v_bfe_u32 v0, v111, 16, 1
	v_bfe_u32 v1, v109, 16, 1
	v_bfe_u32 v2, v107, 16, 1
	v_add3_u32 v3, v105, v3, s55
	v_add3_u32 v7, v110, v7, s55
	v_add3_u32 v6, v108, v6, s55
	v_add3_u32 v5, v106, v5, s55
	v_lshrrev_b32_e32 v4, 16, v4
	v_add3_u32 v2, v107, v2, s55
	v_add3_u32 v1, v109, v1, s55
	v_add3_u32 v0, v111, v0, s55
	v_lshrrev_b32_e32 v5, 16, v5
	v_lshrrev_b32_e32 v6, 16, v6
	v_lshrrev_b32_e32 v7, 16, v7
	v_and_or_b32 v76, v3, s53, v4
	v_bfe_u32 v4, v112, 16, 1
	v_and_or_b32 v79, v0, s53, v7
	v_and_or_b32 v78, v1, s53, v6
	v_and_or_b32 v77, v2, s53, v5
	v_bfe_u32 v3, v113, 16, 1
	v_bfe_u32 v5, v114, 16, 1
	v_bfe_u32 v6, v116, 16, 1
	v_bfe_u32 v7, v118, 16, 1
	v_add3_u32 v4, v112, v4, s55
	v_bfe_u32 v0, v119, 16, 1
	v_bfe_u32 v1, v117, 16, 1
	v_bfe_u32 v2, v115, 16, 1
	v_add3_u32 v3, v113, v3, s55
	v_add3_u32 v7, v118, v7, s55
	v_add3_u32 v6, v116, v6, s55
	v_add3_u32 v5, v114, v5, s55
	v_lshrrev_b32_e32 v4, 16, v4
	v_add3_u32 v2, v115, v2, s55
	v_add3_u32 v1, v117, v1, s55
	v_add3_u32 v0, v119, v0, s55
	v_lshrrev_b32_e32 v5, 16, v5
	v_lshrrev_b32_e32 v6, 16, v6
	v_lshrrev_b32_e32 v7, 16, v7
	v_and_or_b32 v84, v3, s53, v4
	v_bfe_u32 v3, v121, 16, 1
	v_and_or_b32 v87, v0, s53, v7
	v_and_or_b32 v86, v1, s53, v6
	v_and_or_b32 v85, v2, s53, v5
	v_add3_u32 v4, v121, v3, s55
	v_bfe_u32 v3, v120, 16, 1
	v_bfe_u32 v5, v122, 16, 1
	v_bfe_u32 v6, v124, 16, 1
	v_bfe_u32 v7, v126, 16, 1
	v_bfe_u32 v0, v127, 16, 1
	v_bfe_u32 v1, v125, 16, 1
	v_bfe_u32 v2, v123, 16, 1
	v_add3_u32 v7, v126, v7, s55
	v_add3_u32 v6, v124, v6, s55
	v_add3_u32 v5, v122, v5, s55
	v_add3_u32 v3, v120, v3, s55
	v_add3_u32 v2, v123, v2, s55
	v_add3_u32 v1, v125, v1, s55
	v_add3_u32 v0, v127, v0, s55
	v_lshrrev_b32_e32 v8, 16, v3
	v_lshrrev_b32_e32 v3, 16, v5
	v_lshrrev_b32_e32 v5, 16, v6
	v_lshrrev_b32_e32 v6, 16, v7
	v_and_or_b32 v91, v0, s53, v6
	v_and_or_b32 v90, v1, s53, v5
	v_and_or_b32 v89, v2, s53, v3
	v_bfe_u32 v0, v162, 2, 2
	v_lshrrev_b32_e32 v1, 3, v162
	v_bfe_u32 v2, v162, 1, 1
	v_and_or_b32 v99, v1, 2, v2
	v_lshlrev_b32_e32 v30, 2, v0
	v_lshrrev_b32_e32 v1, 4, v162
	v_and_b32_e32 v96, 2, v1
	v_lshlrev_b32_e32 v1, 3, v162
	v_lshl_or_b32 v103, v163, 1, v30
	v_and_b32_e32 v100, 8, v1
	v_bitop3_b32 v1, v30, v99, v96 bitop3:0x36
	v_or_b32_e32 v0, v160, v0
	v_bitop3_b32 v2, v103, v99, 1 bitop3:0x36
	v_add_u32_e32 v101, s49, v100
	v_lshlrev_b32_e32 v1, 4, v1
	v_lshlrev_b32_e32 v102, 8, v0
	v_lshl_add_u32 v2, v2, 4, s49
	v_add3_u32 v116, v101, v1, v102
	v_add3_u32 v117, v2, v102, v100
	ds_read_b64_tr_b16 v[0:1], v116
	ds_read_b64_tr_b16 v[2:3], v117 offset:1024
	v_and_or_b32 v88, v4, s53, v8
	s_waitcnt lgkmcnt(0)
; #define LAS __attribute__((address_space(3)))
; __device__ __forceinline__ unsigned pk2(float lo, float hi) { return f2bf(lo) | (f2bf(hi) << 16); }
; __device__ __forceinline__ void memattn_unit(LAS unsigned char* lds, const bf16* PROJ, const bf16* MKVl, bf16* BR, int b, int hd, int qblk, int tid) {
;     ...
;     const float inv = 1.f / sum;
;     ...
;     bf16* orow = BR + tok * 2048 + 1536 + hd * 128;
; #pragma unroll
;     for (int c = 0; c < 4; ++c) { f32x16 o;
; #pragma unroll
;         for (int i = 0; i < 16; ++i) o[i] = 0.f;
; #pragma unroll
;         for (int ks = 0; ks < 16; ++ks) {
;             const v4i16_t lo = __builtin_amdgcn_ds_read_tr16_b64_v4i16((LAS v4i16_t*)(vimg + kv_off(16u * ks + 8u * hh + q4, 4u * c + 2u * blk + (p >> 1)) + 8u * (p & 1u)));
;             const v4i16_t hi = __builtin_amdgcn_ds_read_tr16_b64_v4i16((LAS v4i16_t*)(vimg + kv_off(16u * ks + 8u * hh + 4u + q4, 4u * c + 2u * blk + (p >> 1)) + 8u * (p & 1u)));
;             const bf16x8 a = __builtin_shufflevector(lo, hi, 0, 1, 2, 3, 4, 5, 6, 7);
;             o = __builtin_amdgcn_mfma_f32_32x32x16_bf16(a, Bp[ks], o, 0, 0, 0); if ((ks & 3) == 3) __builtin_amdgcn_sched_barrier(0); }
; #pragma unroll
;         for (int i4 = 0; i4 < 4; ++i4) { v2u w; w.x = pk2(o[4 * i4] * inv, o[4 * i4 + 1] * inv); w.y = pk2(o[4 * i4 + 2] * inv, o[4 * i4 + 3] * inv);
;             *(v2u*)(orow + 32 * c + 8 * i4 + 4 * hh) = w; } }
	v_mfma_f32_32x32x16_bf16 v[4:19], v[0:3], v[52:55], 0
	v_bfe_u32 v0, v27, 16, 1
	v_bfe_u32 v1, v26, 16, 1
	v_bfe_u32 v2, v24, 16, 1
	v_bfe_u32 v3, v22, 16, 1
	v_add3_u32 v3, v22, v3, s55
	v_add3_u32 v2, v24, v2, s55
	v_add3_u32 v1, v26, v1, s55
	v_add3_u32 v0, v27, v0, s55
	v_bfe_u32 v22, v20, 16, 1
	v_bfe_u32 v24, v21, 16, 1
	v_bfe_u32 v26, v23, 16, 1
	v_bfe_u32 v27, v25, 16, 1
	ds_read_b64_tr_b16 v[104:105], v116 offset:4096
	ds_read_b64_tr_b16 v[108:109], v116 offset:8192
	ds_read_b64_tr_b16 v[112:113], v116 offset:12288
	ds_read_b64_tr_b16 v[106:107], v117 offset:5120
	ds_read_b64_tr_b16 v[110:111], v117 offset:9216
	ds_read_b64_tr_b16 v[114:115], v117 offset:13312
	v_add3_u32 v25, v25, v27, s55
	v_add3_u32 v23, v23, v26, s55
	v_add3_u32 v21, v21, v24, s55
	v_add3_u32 v20, v20, v22, s55
	v_lshrrev_b32_e32 v20, 16, v20
	v_lshrrev_b32_e32 v21, 16, v21
	v_lshrrev_b32_e32 v22, 16, v23
	v_lshrrev_b32_e32 v23, 16, v25
	v_and_or_b32 v95, v0, s53, v23
	v_and_or_b32 v94, v1, s53, v22
	v_and_or_b32 v93, v2, s53, v21
	v_and_or_b32 v92, v3, s53, v20
	v_div_scale_f32 v28, s[0:1], v31, v31, 1.0
	s_waitcnt lgkmcnt(2)
	v_mfma_f32_32x32x16_bf16 v[4:19], v[104:107], v[92:95], v[4:19]
	v_rcp_f32_e32 v29, v28
	v_div_scale_f32 v0, vcc, 1.0, v31, 1.0
	v_or_b32_e32 v104, v30, v96
	v_fma_f32 v97, -v28, v29, 1.0
	v_fmac_f32_e32 v29, v97, v29
	v_mul_f32_e32 v1, v0, v29
	s_waitcnt lgkmcnt(1)
	v_mfma_f32_32x32x16_bf16 v[4:19], v[108:111], v[56:59], v[4:19]
	v_fma_f32 v2, -v28, v1, v0
	v_fmac_f32_e32 v1, v2, v29
	v_fma_f32 v0, -v28, v1, v0
	v_div_fmas_f32 v0, v0, v29, v1
	v_div_fixup_f32 v98, v0, v31, 1.0
	v_lshlrev_b64 v[0:1], 12, v[158:159]
	v_lshl_add_u64 v[0:1], s[16:17], 0, v[0:1]
	v_lshl_add_u64 v[0:1], v[0:1], 0, s[22:23]
	v_lshl_add_u64 v[96:97], v[0:1], 0, v[160:161]
	s_waitcnt lgkmcnt(0)
	v_mfma_f32_32x32x16_bf16 v[4:19], v[112:115], v[40:43], v[4:19]
	ds_read_b64_tr_b16 v[2:3], v117 offset:17408
	ds_read_b64_tr_b16 v[0:1], v116 offset:16384
	ds_read_b64_tr_b16 v[20:21], v116 offset:20480
	ds_read_b64_tr_b16 v[24:25], v116 offset:24576
	ds_read_b64_tr_b16 v[28:29], v116 offset:28672
	ds_read_b64_tr_b16 v[22:23], v117 offset:21504
	ds_read_b64_tr_b16 v[26:27], v117 offset:25600
	ds_read_b64_tr_b16 v[30:31], v117 offset:29696
	s_waitcnt lgkmcnt(6)
	v_mfma_f32_32x32x16_bf16 v[4:19], v[0:3], v[32:35], v[4:19]
	s_waitcnt lgkmcnt(2)
	v_mfma_f32_32x32x16_bf16 v[4:19], v[20:23], v[36:39], v[4:19]
	s_waitcnt lgkmcnt(1)
	v_mfma_f32_32x32x16_bf16 v[4:19], v[24:27], v[48:51], v[4:19]
	s_waitcnt lgkmcnt(0)
	v_mfma_f32_32x32x16_bf16 v[4:19], v[28:31], v[64:67], v[4:19]
	ds_read_b64_tr_b16 v[2:3], v117 offset:33792
	ds_read_b64_tr_b16 v[0:1], v116 offset:32768
	ds_read_b64_tr_b16 v[20:21], v116 offset:36864
	ds_read_b64_tr_b16 v[24:25], v116 offset:40960
	ds_read_b64_tr_b16 v[28:29], v116 offset:45056
	ds_read_b64_tr_b16 v[22:23], v117 offset:37888
	ds_read_b64_tr_b16 v[26:27], v117 offset:41984
	ds_read_b64_tr_b16 v[30:31], v117 offset:46080
	s_waitcnt lgkmcnt(6)
	v_mfma_f32_32x32x16_bf16 v[4:19], v[0:3], v[44:47], v[4:19]
	s_waitcnt lgkmcnt(2)
	v_mfma_f32_32x32x16_bf16 v[4:19], v[20:23], v[60:63], v[4:19]
	s_waitcnt lgkmcnt(1)
	v_mfma_f32_32x32x16_bf16 v[4:19], v[24:27], v[72:75], v[4:19]
	s_waitcnt lgkmcnt(0)
	v_mfma_f32_32x32x16_bf16 v[4:19], v[28:31], v[80:83], v[4:19]
	ds_read_b64_tr_b16 v[2:3], v117 offset:50176
	ds_read_b64_tr_b16 v[0:1], v116 offset:49152
	ds_read_b64_tr_b16 v[20:21], v116 offset:53248
	ds_read_b64_tr_b16 v[24:25], v116 offset:57344
	ds_read_b64_tr_b16 v[28:29], v116 offset:61440
	ds_read_b64_tr_b16 v[22:23], v117 offset:54272
	ds_read_b64_tr_b16 v[26:27], v117 offset:58368
	ds_read_b64_tr_b16 v[30:31], v117 offset:62464
	s_waitcnt lgkmcnt(6)
	v_mfma_f32_32x32x16_bf16 v[4:19], v[0:3], v[68:71], v[4:19]
	s_waitcnt lgkmcnt(2)
	v_mfma_f32_32x32x16_bf16 v[4:19], v[20:23], v[76:79], v[4:19]
	s_waitcnt lgkmcnt(1)
	v_mfma_f32_32x32x16_bf16 v[4:19], v[24:27], v[84:87], v[4:19]
	s_waitcnt lgkmcnt(0)
	v_mfma_f32_32x32x16_bf16 v[4:19], v[28:31], v[88:91], v[4:19]
	s_nop 11
	v_mov_b32_e32 v0, v4
	v_mov_b32_e32 v1, v6
	v_pk_mul_f32 v[0:1], v[0:1], v[98:99] op_sel_hi:[1,0]
	v_mov_b32_e32 v6, v5
	v_pk_mul_f32 v[2:3], v[6:7], v[98:99] op_sel_hi:[1,0]
	v_and_b32_sdwa v4, v1, v248 dst_sel:DWORD dst_unused:UNUSED_PAD src0_sel:WORD_1 src1_sel:DWORD
	v_and_b32_sdwa v5, v0, v248 dst_sel:DWORD dst_unused:UNUSED_PAD src0_sel:WORD_1 src1_sel:DWORD
	v_add3_u32 v0, v0, v5, s55
	v_add3_u32 v1, v1, v4, s55
	v_and_b32_sdwa v4, v3, v248 dst_sel:DWORD dst_unused:UNUSED_PAD src0_sel:WORD_1 src1_sel:DWORD
	v_and_b32_sdwa v5, v2, v248 dst_sel:DWORD dst_unused:UNUSED_PAD src0_sel:WORD_1 src1_sel:DWORD
	v_add3_u32 v3, v3, v4, s55
	v_add3_u32 v2, v2, v5, s55
	v_and_b32_e32 v3, 0xffff0000, v3
	v_and_b32_e32 v2, 0xffff0000, v2
	v_or_b32_sdwa v1, v3, v1 dst_sel:DWORD dst_unused:UNUSED_PAD src0_sel:DWORD src1_sel:WORD_1
	v_or_b32_sdwa v0, v2, v0 dst_sel:DWORD dst_unused:UNUSED_PAD src0_sel:DWORD src1_sel:WORD_1
	global_store_dwordx2 v[96:97], v[0:1], off offset:3072
	v_mov_b32_e32 v0, v8
	v_mov_b32_e32 v1, v10
	v_pk_mul_f32 v[0:1], v[0:1], v[98:99] op_sel_hi:[1,0]
	v_mov_b32_e32 v10, v9
	v_pk_mul_f32 v[2:3], v[10:11], v[98:99] op_sel_hi:[1,0]
	v_and_b32_sdwa v4, v1, v248 dst_sel:DWORD dst_unused:UNUSED_PAD src0_sel:WORD_1 src1_sel:DWORD
	v_and_b32_sdwa v5, v0, v248 dst_sel:DWORD dst_unused:UNUSED_PAD src0_sel:WORD_1 src1_sel:DWORD
	v_add3_u32 v0, v0, v5, s55
	v_add3_u32 v1, v1, v4, s55
	v_and_b32_sdwa v4, v3, v248 dst_sel:DWORD dst_unused:UNUSED_PAD src0_sel:WORD_1 src1_sel:DWORD
	v_and_b32_sdwa v5, v2, v248 dst_sel:DWORD dst_unused:UNUSED_PAD src0_sel:WORD_1 src1_sel:DWORD
; #define LAS __attribute__((address_space(3)))
; __device__ __forceinline__ unsigned pk2(float lo, float hi) { return f2bf(lo) | (f2bf(hi) << 16); }
; __device__ __forceinline__ void memattn_unit(LAS unsigned char* lds, const bf16* PROJ, const bf16* MKVl, bf16* BR, int b, int hd, int qblk, int tid) {
;     ...
;     for (int c = 0; c < 4; ++c) { f32x16 o;
; #pragma unroll
;         for (int i = 0; i < 16; ++i) o[i] = 0.f;
; #pragma unroll
;         for (int ks = 0; ks < 16; ++ks) {
;             const v4i16_t lo = __builtin_amdgcn_ds_read_tr16_b64_v4i16((LAS v4i16_t*)(vimg + kv_off(16u * ks + 8u * hh + q4, 4u * c + 2u * blk + (p >> 1)) + 8u * (p & 1u)));
;             const v4i16_t hi = __builtin_amdgcn_ds_read_tr16_b64_v4i16((LAS v4i16_t*)(vimg + kv_off(16u * ks + 8u * hh + 4u + q4, 4u * c + 2u * blk + (p >> 1)) + 8u * (p & 1u)));
;             const bf16x8 a = __builtin_shufflevector(lo, hi, 0, 1, 2, 3, 4, 5, 6, 7);
;             o = __builtin_amdgcn_mfma_f32_32x32x16_bf16(a, Bp[ks], o, 0, 0, 0); if ((ks & 3) == 3) __builtin_amdgcn_sched_barrier(0); }
; #pragma unroll
;         for (int i4 = 0; i4 < 4; ++i4) { v2u w; w.x = pk2(o[4 * i4] * inv, o[4 * i4 + 1] * inv); w.y = pk2(o[4 * i4 + 2] * inv, o[4 * i4 + 3] * inv);
;             *(v2u*)(orow + 32 * c + 8 * i4 + 4 * hh) = w; } }
	v_add3_u32 v3, v3, v4, s55
	v_add3_u32 v2, v2, v5, s55
	v_and_b32_e32 v3, 0xffff0000, v3
	v_and_b32_e32 v2, 0xffff0000, v2
	v_or_b32_sdwa v1, v3, v1 dst_sel:DWORD dst_unused:UNUSED_PAD src0_sel:DWORD src1_sel:WORD_1
	v_or_b32_sdwa v0, v2, v0 dst_sel:DWORD dst_unused:UNUSED_PAD src0_sel:DWORD src1_sel:WORD_1
	global_store_dwordx2 v[96:97], v[0:1], off offset:3088
	v_mov_b32_e32 v0, v12
	v_mov_b32_e32 v1, v14
	v_pk_mul_f32 v[0:1], v[0:1], v[98:99] op_sel_hi:[1,0]
	v_mov_b32_e32 v14, v13
	v_pk_mul_f32 v[2:3], v[14:15], v[98:99] op_sel_hi:[1,0]
	v_and_b32_sdwa v4, v1, v248 dst_sel:DWORD dst_unused:UNUSED_PAD src0_sel:WORD_1 src1_sel:DWORD
	v_and_b32_sdwa v5, v0, v248 dst_sel:DWORD dst_unused:UNUSED_PAD src0_sel:WORD_1 src1_sel:DWORD
	v_add3_u32 v106, v1, v4, s55
	v_and_b32_sdwa v1, v2, v248 dst_sel:DWORD dst_unused:UNUSED_PAD src0_sel:WORD_1 src1_sel:DWORD
	v_add3_u32 v105, v0, v5, s55
	v_and_b32_sdwa v0, v3, v248 dst_sel:DWORD dst_unused:UNUSED_PAD src0_sel:WORD_1 src1_sel:DWORD
	v_add3_u32 v5, v2, v1, s55
	v_or_b32_e32 v2, 4, v99
	v_add3_u32 v4, v3, v0, s55
	v_bitop3_b32 v0, v99, v104, 4 bitop3:0x36
	v_bitop3_b32 v2, v103, v2, 1 bitop3:0x36
	v_lshlrev_b32_e32 v0, 4, v0
	v_lshl_add_u32 v2, v2, 4, s49
	v_add3_u32 v108, v101, v0, v102
	v_add3_u32 v109, v2, v102, v100
	ds_read_b64_tr_b16 v[0:1], v108
	ds_read_b64_tr_b16 v[2:3], v109 offset:1024
	v_and_b32_e32 v107, 0xffff0000, v4
	v_and_b32_e32 v110, 0xffff0000, v5
	s_waitcnt lgkmcnt(0)
	v_mfma_f32_32x32x16_bf16 v[0:15], v[0:3], v[52:55], 0
	ds_read_b64_tr_b16 v[20:21], v108 offset:4096
	ds_read_b64_tr_b16 v[24:25], v108 offset:8192
	ds_read_b64_tr_b16 v[28:29], v108 offset:12288
	ds_read_b64_tr_b16 v[22:23], v109 offset:5120
	ds_read_b64_tr_b16 v[26:27], v109 offset:9216
	ds_read_b64_tr_b16 v[30:31], v109 offset:13312
	v_or_b32_sdwa v107, v107, v106 dst_sel:DWORD dst_unused:UNUSED_PAD src0_sel:DWORD src1_sel:WORD_1
	v_or_b32_sdwa v106, v110, v105 dst_sel:DWORD dst_unused:UNUSED_PAD src0_sel:DWORD src1_sel:WORD_1
	global_store_dwordx2 v[96:97], v[106:107], off offset:3104
	v_mov_b32_e32 v107, v18
	v_mov_b32_e32 v18, v17
	v_mov_b32_e32 v106, v16
	s_waitcnt lgkmcnt(2)
	v_mfma_f32_32x32x16_bf16 v[0:15], v[20:23], v[92:95], v[0:15]
	v_mul_f32_e64 v16, v18, v98
	v_mul_f32_e64 v17, v19, v98
	v_mul_f32_e64 v106, v106, v98
	v_mul_f32_e64 v107, v107, v98
	v_and_b32_sdwa v20, v17, v248 dst_sel:DWORD dst_unused:UNUSED_PAD src0_sel:WORD_1 src1_sel:DWORD
	v_and_b32_sdwa v21, v16, v248 dst_sel:DWORD dst_unused:UNUSED_PAD src0_sel:WORD_1 src1_sel:DWORD
	v_and_b32_sdwa v18, v107, v248 dst_sel:DWORD dst_unused:UNUSED_PAD src0_sel:WORD_1 src1_sel:DWORD
	v_and_b32_sdwa v19, v106, v248 dst_sel:DWORD dst_unused:UNUSED_PAD src0_sel:WORD_1 src1_sel:DWORD
	v_add3_u32 v17, v17, v20, s55
	s_waitcnt lgkmcnt(1)
	v_mfma_f32_32x32x16_bf16 v[0:15], v[24:27], v[56:59], v[0:15]
	v_add3_u32 v16, v16, v21, s55
	v_add3_u32 v19, v106, v19, s55
	v_add3_u32 v18, v107, v18, s55
	v_and_b32_e32 v17, 0xffff0000, v17
	v_and_b32_e32 v16, 0xffff0000, v16
	v_or_b32_sdwa v17, v17, v18 dst_sel:DWORD dst_unused:UNUSED_PAD src0_sel:DWORD src1_sel:WORD_1
	v_or_b32_sdwa v16, v16, v19 dst_sel:DWORD dst_unused:UNUSED_PAD src0_sel:DWORD src1_sel:WORD_1
	global_store_dwordx2 v[96:97], v[16:17], off offset:3120
	s_waitcnt lgkmcnt(0)
	v_mfma_f32_32x32x16_bf16 v[0:15], v[28:31], v[40:43], v[0:15]
	ds_read_b64_tr_b16 v[18:19], v109 offset:17408
	ds_read_b64_tr_b16 v[16:17], v108 offset:16384
	ds_read_b64_tr_b16 v[20:21], v108 offset:20480
	ds_read_b64_tr_b16 v[24:25], v108 offset:24576
	ds_read_b64_tr_b16 v[28:29], v108 offset:28672
	ds_read_b64_tr_b16 v[22:23], v109 offset:21504
	ds_read_b64_tr_b16 v[26:27], v109 offset:25600
	ds_read_b64_tr_b16 v[30:31], v109 offset:29696
	s_waitcnt lgkmcnt(6)
	v_mfma_f32_32x32x16_bf16 v[0:15], v[16:19], v[32:35], v[0:15]
	s_waitcnt lgkmcnt(2)
	v_mfma_f32_32x32x16_bf16 v[0:15], v[20:23], v[36:39], v[0:15]
	s_waitcnt lgkmcnt(1)
	v_mfma_f32_32x32x16_bf16 v[0:15], v[24:27], v[48:51], v[0:15]
	s_waitcnt lgkmcnt(0)
	v_mfma_f32_32x32x16_bf16 v[0:15], v[28:31], v[64:67], v[0:15]
	ds_read_b64_tr_b16 v[18:19], v109 offset:33792
	ds_read_b64_tr_b16 v[16:17], v108 offset:32768
	ds_read_b64_tr_b16 v[20:21], v108 offset:36864
	ds_read_b64_tr_b16 v[24:25], v108 offset:40960
	ds_read_b64_tr_b16 v[28:29], v108 offset:45056
	ds_read_b64_tr_b16 v[22:23], v109 offset:37888
	ds_read_b64_tr_b16 v[26:27], v109 offset:41984
	ds_read_b64_tr_b16 v[30:31], v109 offset:46080
	s_waitcnt lgkmcnt(6)
	v_mfma_f32_32x32x16_bf16 v[0:15], v[16:19], v[44:47], v[0:15]
	s_waitcnt lgkmcnt(2)
	v_mfma_f32_32x32x16_bf16 v[0:15], v[20:23], v[60:63], v[0:15]
	s_waitcnt lgkmcnt(1)
	v_mfma_f32_32x32x16_bf16 v[0:15], v[24:27], v[72:75], v[0:15]
	s_waitcnt lgkmcnt(0)
	v_mfma_f32_32x32x16_bf16 v[0:15], v[28:31], v[80:83], v[0:15]
	ds_read_b64_tr_b16 v[18:19], v109 offset:50176
	ds_read_b64_tr_b16 v[16:17], v108 offset:49152
	ds_read_b64_tr_b16 v[20:21], v108 offset:53248
	ds_read_b64_tr_b16 v[24:25], v108 offset:57344
	ds_read_b64_tr_b16 v[28:29], v108 offset:61440
	ds_read_b64_tr_b16 v[22:23], v109 offset:54272
	ds_read_b64_tr_b16 v[26:27], v109 offset:58368
	ds_read_b64_tr_b16 v[30:31], v109 offset:62464
	s_waitcnt lgkmcnt(6)
	v_mfma_f32_32x32x16_bf16 v[0:15], v[16:19], v[68:71], v[0:15]
	s_waitcnt lgkmcnt(2)
	v_mfma_f32_32x32x16_bf16 v[0:15], v[20:23], v[76:79], v[0:15]
	s_waitcnt lgkmcnt(1)
	v_mfma_f32_32x32x16_bf16 v[0:15], v[24:27], v[84:87], v[0:15]
	s_waitcnt lgkmcnt(0)
; #define LAS __attribute__((address_space(3)))
; __device__ __forceinline__ unsigned pk2(float lo, float hi) { return f2bf(lo) | (f2bf(hi) << 16); }
; __device__ __forceinline__ void memattn_unit(LAS unsigned char* lds, const bf16* PROJ, const bf16* MKVl, bf16* BR, int b, int hd, int qblk, int tid) {
;     ...
;     for (int c = 0; c < 4; ++c) { f32x16 o;
; #pragma unroll
;         for (int i = 0; i < 16; ++i) o[i] = 0.f;
; #pragma unroll
;         for (int ks = 0; ks < 16; ++ks) {
;             const v4i16_t lo = __builtin_amdgcn_ds_read_tr16_b64_v4i16((LAS v4i16_t*)(vimg + kv_off(16u * ks + 8u * hh + q4, 4u * c + 2u * blk + (p >> 1)) + 8u * (p & 1u)));
;             const v4i16_t hi = __builtin_amdgcn_ds_read_tr16_b64_v4i16((LAS v4i16_t*)(vimg + kv_off(16u * ks + 8u * hh + 4u + q4, 4u * c + 2u * blk + (p >> 1)) + 8u * (p & 1u)));
;             const bf16x8 a = __builtin_shufflevector(lo, hi, 0, 1, 2, 3, 4, 5, 6, 7);
;             o = __builtin_amdgcn_mfma_f32_32x32x16_bf16(a, Bp[ks], o, 0, 0, 0); if ((ks & 3) == 3) __builtin_amdgcn_sched_barrier(0); }
; #pragma unroll
;         for (int i4 = 0; i4 < 4; ++i4) { v2u w; w.x = pk2(o[4 * i4] * inv, o[4 * i4 + 1] * inv); w.y = pk2(o[4 * i4 + 2] * inv, o[4 * i4 + 3] * inv);
;             *(v2u*)(orow + 32 * c + 8 * i4 + 4 * hh) = w; } }
	v_mfma_f32_32x32x16_bf16 v[0:15], v[28:31], v[88:91], v[0:15]
	s_nop 11
	v_mov_b32_e32 v16, v0
	v_mov_b32_e32 v17, v2
	v_pk_mul_f32 v[16:17], v[16:17], v[98:99] op_sel_hi:[1,0]
	v_mov_b32_e32 v2, v1
	v_pk_mul_f32 v[0:1], v[2:3], v[98:99] op_sel_hi:[1,0]
	v_and_b32_sdwa v2, v17, v248 dst_sel:DWORD dst_unused:UNUSED_PAD src0_sel:WORD_1 src1_sel:DWORD
	v_and_b32_sdwa v3, v16, v248 dst_sel:DWORD dst_unused:UNUSED_PAD src0_sel:WORD_1 src1_sel:DWORD
	v_add3_u32 v3, v16, v3, s55
	v_add3_u32 v2, v17, v2, s55
	v_and_b32_sdwa v16, v1, v248 dst_sel:DWORD dst_unused:UNUSED_PAD src0_sel:WORD_1 src1_sel:DWORD
	v_and_b32_sdwa v17, v0, v248 dst_sel:DWORD dst_unused:UNUSED_PAD src0_sel:WORD_1 src1_sel:DWORD
	v_add3_u32 v1, v1, v16, s55
	v_add3_u32 v0, v0, v17, s55
	v_and_b32_e32 v1, 0xffff0000, v1
	v_and_b32_e32 v0, 0xffff0000, v0
	v_or_b32_sdwa v1, v1, v2 dst_sel:DWORD dst_unused:UNUSED_PAD src0_sel:DWORD src1_sel:WORD_1
	v_or_b32_sdwa v0, v0, v3 dst_sel:DWORD dst_unused:UNUSED_PAD src0_sel:DWORD src1_sel:WORD_1
	global_store_dwordx2 v[96:97], v[0:1], off offset:3136
	v_mov_b32_e32 v0, v4
	v_mov_b32_e32 v1, v6
	v_pk_mul_f32 v[0:1], v[0:1], v[98:99] op_sel_hi:[1,0]
	v_mov_b32_e32 v6, v5
	v_pk_mul_f32 v[2:3], v[6:7], v[98:99] op_sel_hi:[1,0]
	v_and_b32_sdwa v4, v1, v248 dst_sel:DWORD dst_unused:UNUSED_PAD src0_sel:WORD_1 src1_sel:DWORD
	v_and_b32_sdwa v5, v0, v248 dst_sel:DWORD dst_unused:UNUSED_PAD src0_sel:WORD_1 src1_sel:DWORD
	v_add3_u32 v0, v0, v5, s55
	v_add3_u32 v1, v1, v4, s55
	v_and_b32_sdwa v4, v3, v248 dst_sel:DWORD dst_unused:UNUSED_PAD src0_sel:WORD_1 src1_sel:DWORD
	v_and_b32_sdwa v5, v2, v248 dst_sel:DWORD dst_unused:UNUSED_PAD src0_sel:WORD_1 src1_sel:DWORD
	v_add3_u32 v3, v3, v4, s55
	v_add3_u32 v2, v2, v5, s55
	v_and_b32_e32 v3, 0xffff0000, v3
	v_and_b32_e32 v2, 0xffff0000, v2
	v_or_b32_sdwa v1, v3, v1 dst_sel:DWORD dst_unused:UNUSED_PAD src0_sel:DWORD src1_sel:WORD_1
	v_or_b32_sdwa v0, v2, v0 dst_sel:DWORD dst_unused:UNUSED_PAD src0_sel:DWORD src1_sel:WORD_1
	global_store_dwordx2 v[96:97], v[0:1], off offset:3152
	v_mov_b32_e32 v0, v8
	v_mov_b32_e32 v1, v10
	v_pk_mul_f32 v[0:1], v[0:1], v[98:99] op_sel_hi:[1,0]
	v_mov_b32_e32 v10, v9
	v_pk_mul_f32 v[2:3], v[10:11], v[98:99] op_sel_hi:[1,0]
	v_and_b32_sdwa v4, v1, v248 dst_sel:DWORD dst_unused:UNUSED_PAD src0_sel:WORD_1 src1_sel:DWORD
	v_and_b32_sdwa v5, v0, v248 dst_sel:DWORD dst_unused:UNUSED_PAD src0_sel:WORD_1 src1_sel:DWORD
	v_add3_u32 v110, v1, v4, s55
	v_and_b32_sdwa v1, v2, v248 dst_sel:DWORD dst_unused:UNUSED_PAD src0_sel:WORD_1 src1_sel:DWORD
	v_add3_u32 v105, v0, v5, s55
	v_and_b32_sdwa v0, v3, v248 dst_sel:DWORD dst_unused:UNUSED_PAD src0_sel:WORD_1 src1_sel:DWORD
	v_add3_u32 v5, v2, v1, s55
	v_or_b32_e32 v2, 8, v99
	v_add3_u32 v4, v3, v0, s55
	v_bitop3_b32 v0, v99, v104, 8 bitop3:0x36
	v_bitop3_b32 v2, v103, v2, 1 bitop3:0x36
	v_lshlrev_b32_e32 v0, 4, v0
	v_lshl_add_u32 v2, v2, 4, s49
	v_add3_u32 v111, v101, v0, v102
	v_add3_u32 v112, v2, v102, v100
	ds_read_b64_tr_b16 v[0:1], v111
	ds_read_b64_tr_b16 v[2:3], v112 offset:1024
	s_waitcnt lgkmcnt(0)
	v_mfma_f32_32x32x16_bf16 v[16:31], v[0:3], v[52:55], 0
	v_and_b32_e32 v113, 0xffff0000, v4
	v_and_b32_e32 v114, 0xffff0000, v5
	ds_read_b64_tr_b16 v[4:5], v111 offset:4096
	ds_read_b64_tr_b16 v[8:9], v111 offset:8192
	ds_read_b64_tr_b16 v[106:107], v111 offset:12288
	ds_read_b64_tr_b16 v[6:7], v112 offset:5120
	ds_read_b64_tr_b16 v[10:11], v112 offset:9216
	ds_read_b64_tr_b16 v[108:109], v112 offset:13312
	v_or_b32_sdwa v1, v113, v110 dst_sel:DWORD dst_unused:UNUSED_PAD src0_sel:DWORD src1_sel:WORD_1
	v_or_b32_sdwa v0, v114, v105 dst_sel:DWORD dst_unused:UNUSED_PAD src0_sel:DWORD src1_sel:WORD_1
	global_store_dwordx2 v[96:97], v[0:1], off offset:3168
	v_mov_b32_e32 v0, v12
	s_waitcnt lgkmcnt(2)
	v_mfma_f32_32x32x16_bf16 v[16:31], v[4:7], v[92:95], v[16:31]
	v_mov_b32_e32 v1, v14
	v_mul_f32_e64 v0, v0, v98
	v_mul_f32_e64 v1, v1, v98
	v_mov_b32_e32 v14, v13
	v_mul_f32_e64 v2, v14, v98
	v_mul_f32_e64 v3, v15, v98
	v_and_b32_sdwa v4, v1, v248 dst_sel:DWORD dst_unused:UNUSED_PAD src0_sel:WORD_1 src1_sel:DWORD
	v_and_b32_sdwa v5, v0, v248 dst_sel:DWORD dst_unused:UNUSED_PAD src0_sel:WORD_1 src1_sel:DWORD
	v_add3_u32 v0, v0, v5, s55
	s_waitcnt lgkmcnt(1)
	v_mfma_f32_32x32x16_bf16 v[16:31], v[8:11], v[56:59], v[16:31]
	v_add3_u32 v1, v1, v4, s55
	v_and_b32_sdwa v4, v3, v248 dst_sel:DWORD dst_unused:UNUSED_PAD src0_sel:WORD_1 src1_sel:DWORD
	v_and_b32_sdwa v5, v2, v248 dst_sel:DWORD dst_unused:UNUSED_PAD src0_sel:WORD_1 src1_sel:DWORD
	v_add3_u32 v3, v3, v4, s55
	v_add3_u32 v2, v2, v5, s55
	v_and_b32_e32 v3, 0xffff0000, v3
	v_and_b32_e32 v2, 0xffff0000, v2
	v_or_b32_sdwa v1, v3, v1 dst_sel:DWORD dst_unused:UNUSED_PAD src0_sel:DWORD src1_sel:WORD_1
	v_or_b32_sdwa v0, v2, v0 dst_sel:DWORD dst_unused:UNUSED_PAD src0_sel:DWORD src1_sel:WORD_1
	global_store_dwordx2 v[96:97], v[0:1], off offset:3184
	s_waitcnt lgkmcnt(0)
	v_mfma_f32_32x32x16_bf16 v[16:31], v[106:109], v[40:43], v[16:31]
	ds_read_b64_tr_b16 v[2:3], v112 offset:17408
	ds_read_b64_tr_b16 v[0:1], v111 offset:16384
	ds_read_b64_tr_b16 v[4:5], v111 offset:20480
	ds_read_b64_tr_b16 v[8:9], v111 offset:24576
	ds_read_b64_tr_b16 v[12:13], v111 offset:28672
	ds_read_b64_tr_b16 v[6:7], v112 offset:21504
	ds_read_b64_tr_b16 v[10:11], v112 offset:25600
	ds_read_b64_tr_b16 v[14:15], v112 offset:29696
	s_waitcnt lgkmcnt(6)
	v_mfma_f32_32x32x16_bf16 v[16:31], v[0:3], v[32:35], v[16:31]
	s_waitcnt lgkmcnt(2)
	v_mfma_f32_32x32x16_bf16 v[16:31], v[4:7], v[36:39], v[16:31]
	s_waitcnt lgkmcnt(1)
	v_mfma_f32_32x32x16_bf16 v[16:31], v[8:11], v[48:51], v[16:31]
	s_waitcnt lgkmcnt(0)
; #define LAS __attribute__((address_space(3)))
; __device__ __forceinline__ unsigned pk2(float lo, float hi) { return f2bf(lo) | (f2bf(hi) << 16); }
; __device__ __forceinline__ void memattn_unit(LAS unsigned char* lds, const bf16* PROJ, const bf16* MKVl, bf16* BR, int b, int hd, int qblk, int tid) {
;     ...
;     for (int c = 0; c < 4; ++c) { f32x16 o;
; #pragma unroll
;         for (int i = 0; i < 16; ++i) o[i] = 0.f;
; #pragma unroll
;         for (int ks = 0; ks < 16; ++ks) {
;             const v4i16_t lo = __builtin_amdgcn_ds_read_tr16_b64_v4i16((LAS v4i16_t*)(vimg + kv_off(16u * ks + 8u * hh + q4, 4u * c + 2u * blk + (p >> 1)) + 8u * (p & 1u)));
;             const v4i16_t hi = __builtin_amdgcn_ds_read_tr16_b64_v4i16((LAS v4i16_t*)(vimg + kv_off(16u * ks + 8u * hh + 4u + q4, 4u * c + 2u * blk + (p >> 1)) + 8u * (p & 1u)));
;             const bf16x8 a = __builtin_shufflevector(lo, hi, 0, 1, 2, 3, 4, 5, 6, 7);
;             o = __builtin_amdgcn_mfma_f32_32x32x16_bf16(a, Bp[ks], o, 0, 0, 0); if ((ks & 3) == 3) __builtin_amdgcn_sched_barrier(0); }
; #pragma unroll
;         for (int i4 = 0; i4 < 4; ++i4) { v2u w; w.x = pk2(o[4 * i4] * inv, o[4 * i4 + 1] * inv); w.y = pk2(o[4 * i4 + 2] * inv, o[4 * i4 + 3] * inv);
;             *(v2u*)(orow + 32 * c + 8 * i4 + 4 * hh) = w; } }
	v_mfma_f32_32x32x16_bf16 v[16:31], v[12:15], v[64:67], v[16:31]
	ds_read_b64_tr_b16 v[2:3], v112 offset:33792
	ds_read_b64_tr_b16 v[0:1], v111 offset:32768
	ds_read_b64_tr_b16 v[4:5], v111 offset:36864
	ds_read_b64_tr_b16 v[8:9], v111 offset:40960
	ds_read_b64_tr_b16 v[12:13], v111 offset:45056
	ds_read_b64_tr_b16 v[6:7], v112 offset:37888
	ds_read_b64_tr_b16 v[10:11], v112 offset:41984
	ds_read_b64_tr_b16 v[14:15], v112 offset:46080
	s_waitcnt lgkmcnt(6)
	v_mfma_f32_32x32x16_bf16 v[16:31], v[0:3], v[44:47], v[16:31]
	s_waitcnt lgkmcnt(2)
	v_mfma_f32_32x32x16_bf16 v[16:31], v[4:7], v[60:63], v[16:31]
	s_waitcnt lgkmcnt(1)
	v_mfma_f32_32x32x16_bf16 v[16:31], v[8:11], v[72:75], v[16:31]
	s_waitcnt lgkmcnt(0)
	v_mfma_f32_32x32x16_bf16 v[16:31], v[12:15], v[80:83], v[16:31]
	ds_read_b64_tr_b16 v[2:3], v112 offset:50176
	ds_read_b64_tr_b16 v[0:1], v111 offset:49152
	ds_read_b64_tr_b16 v[4:5], v111 offset:53248
	ds_read_b64_tr_b16 v[8:9], v111 offset:57344
	ds_read_b64_tr_b16 v[12:13], v111 offset:61440
	ds_read_b64_tr_b16 v[6:7], v112 offset:54272
	ds_read_b64_tr_b16 v[10:11], v112 offset:58368
	ds_read_b64_tr_b16 v[14:15], v112 offset:62464
	s_waitcnt lgkmcnt(6)
	v_mfma_f32_32x32x16_bf16 v[16:31], v[0:3], v[68:71], v[16:31]
	s_waitcnt lgkmcnt(2)
	v_mfma_f32_32x32x16_bf16 v[16:31], v[4:7], v[76:79], v[16:31]
	s_waitcnt lgkmcnt(1)
	v_mfma_f32_32x32x16_bf16 v[16:31], v[8:11], v[84:87], v[16:31]
	s_waitcnt lgkmcnt(0)
	v_mfma_f32_32x32x16_bf16 v[16:31], v[12:15], v[88:91], v[16:31]
	s_nop 11
	v_mov_b32_e32 v0, v16
	v_mov_b32_e32 v1, v18
	v_pk_mul_f32 v[0:1], v[98:99], v[0:1] op_sel_hi:[0,1]
	v_mov_b32_e32 v18, v17
	v_pk_mul_f32 v[2:3], v[98:99], v[18:19] op_sel_hi:[0,1]
	v_and_b32_sdwa v4, v1, v248 dst_sel:DWORD dst_unused:UNUSED_PAD src0_sel:WORD_1 src1_sel:DWORD
	v_and_b32_sdwa v5, v0, v248 dst_sel:DWORD dst_unused:UNUSED_PAD src0_sel:WORD_1 src1_sel:DWORD
	v_add3_u32 v0, v0, v5, s55
	v_add3_u32 v1, v1, v4, s55
	v_and_b32_sdwa v4, v3, v248 dst_sel:DWORD dst_unused:UNUSED_PAD src0_sel:WORD_1 src1_sel:DWORD
	v_and_b32_sdwa v5, v2, v248 dst_sel:DWORD dst_unused:UNUSED_PAD src0_sel:WORD_1 src1_sel:DWORD
	v_add3_u32 v3, v3, v4, s55
	v_add3_u32 v2, v2, v5, s55
	v_and_b32_e32 v3, 0xffff0000, v3
	v_and_b32_e32 v2, 0xffff0000, v2
	v_or_b32_sdwa v1, v3, v1 dst_sel:DWORD dst_unused:UNUSED_PAD src0_sel:DWORD src1_sel:WORD_1
	v_or_b32_sdwa v0, v2, v0 dst_sel:DWORD dst_unused:UNUSED_PAD src0_sel:DWORD src1_sel:WORD_1
	global_store_dwordx2 v[96:97], v[0:1], off offset:3200
	v_mov_b32_e32 v0, v20
	v_mov_b32_e32 v1, v22
	v_pk_mul_f32 v[0:1], v[98:99], v[0:1] op_sel_hi:[0,1]
	v_mov_b32_e32 v22, v21
	v_pk_mul_f32 v[2:3], v[98:99], v[22:23] op_sel_hi:[0,1]
	v_and_b32_sdwa v4, v1, v248 dst_sel:DWORD dst_unused:UNUSED_PAD src0_sel:WORD_1 src1_sel:DWORD
	v_and_b32_sdwa v5, v0, v248 dst_sel:DWORD dst_unused:UNUSED_PAD src0_sel:WORD_1 src1_sel:DWORD
	v_add3_u32 v0, v0, v5, s55
	v_add3_u32 v1, v1, v4, s55
	v_and_b32_sdwa v4, v3, v248 dst_sel:DWORD dst_unused:UNUSED_PAD src0_sel:WORD_1 src1_sel:DWORD
	v_and_b32_sdwa v5, v2, v248 dst_sel:DWORD dst_unused:UNUSED_PAD src0_sel:WORD_1 src1_sel:DWORD
	v_add3_u32 v3, v3, v4, s55
	v_add3_u32 v2, v2, v5, s55
	v_and_b32_e32 v3, 0xffff0000, v3
	v_and_b32_e32 v2, 0xffff0000, v2
	v_or_b32_sdwa v1, v3, v1 dst_sel:DWORD dst_unused:UNUSED_PAD src0_sel:DWORD src1_sel:WORD_1
	v_or_b32_sdwa v0, v2, v0 dst_sel:DWORD dst_unused:UNUSED_PAD src0_sel:DWORD src1_sel:WORD_1
	global_store_dwordx2 v[96:97], v[0:1], off offset:3216
	v_mov_b32_e32 v0, v24
	v_mov_b32_e32 v1, v26
	v_pk_mul_f32 v[0:1], v[98:99], v[0:1] op_sel_hi:[0,1]
	v_mov_b32_e32 v26, v25
	v_pk_mul_f32 v[2:3], v[98:99], v[26:27] op_sel_hi:[0,1]
	v_and_b32_sdwa v4, v1, v248 dst_sel:DWORD dst_unused:UNUSED_PAD src0_sel:WORD_1 src1_sel:DWORD
	v_and_b32_sdwa v5, v0, v248 dst_sel:DWORD dst_unused:UNUSED_PAD src0_sel:WORD_1 src1_sel:DWORD
	v_add3_u32 v106, v1, v4, s55
	v_and_b32_sdwa v1, v2, v248 dst_sel:DWORD dst_unused:UNUSED_PAD src0_sel:WORD_1 src1_sel:DWORD
	v_add3_u32 v105, v0, v5, s55
	v_and_b32_sdwa v0, v3, v248 dst_sel:DWORD dst_unused:UNUSED_PAD src0_sel:WORD_1 src1_sel:DWORD
	v_add3_u32 v5, v2, v1, s55
	v_or_b32_e32 v2, 12, v99
	v_add3_u32 v4, v3, v0, s55
	v_bitop3_b32 v0, v99, v104, 12 bitop3:0x36
	v_bitop3_b32 v2, v103, v2, 1 bitop3:0x36
	v_lshlrev_b32_e32 v0, 4, v0
	v_lshl_add_u32 v2, v2, 4, s49
	v_add3_u32 v99, v101, v0, v102
	v_add3_u32 v100, v2, v102, v100
	ds_read_b64_tr_b16 v[0:1], v99
	ds_read_b64_tr_b16 v[2:3], v100 offset:1024
	v_and_b32_e32 v101, 0xffff0000, v4
	v_and_b32_e32 v102, 0xffff0000, v5
	s_waitcnt lgkmcnt(0)
	v_mfma_f32_32x32x16_bf16 v[0:15], v[0:3], v[52:55], 0
	ds_read_b64_tr_b16 v[16:17], v99 offset:4096
	ds_read_b64_tr_b16 v[20:21], v99 offset:8192
	ds_read_b64_tr_b16 v[24:25], v99 offset:12288
	ds_read_b64_tr_b16 v[18:19], v100 offset:5120
	ds_read_b64_tr_b16 v[22:23], v100 offset:9216
	ds_read_b64_tr_b16 v[26:27], v100 offset:13312
	v_or_b32_sdwa v53, v101, v106 dst_sel:DWORD dst_unused:UNUSED_PAD src0_sel:DWORD src1_sel:WORD_1
	v_or_b32_sdwa v52, v102, v105 dst_sel:DWORD dst_unused:UNUSED_PAD src0_sel:DWORD src1_sel:WORD_1
	global_store_dwordx2 v[96:97], v[52:53], off offset:3232
	v_mov_b32_e32 v53, v30
	v_mov_b32_e32 v30, v29
	v_mov_b32_e32 v52, v28
	s_waitcnt lgkmcnt(2)
	v_mfma_f32_32x32x16_bf16 v[0:15], v[16:19], v[92:95], v[0:15]
	v_mul_f32_e64 v16, v98, v30
	v_mul_f32_e64 v17, v98, v31
	v_mul_f32_e64 v52, v98, v52
	v_mul_f32_e64 v53, v98, v53
	v_and_b32_sdwa v28, v17, v248 dst_sel:DWORD dst_unused:UNUSED_PAD src0_sel:WORD_1 src1_sel:DWORD
	v_and_b32_sdwa v29, v16, v248 dst_sel:DWORD dst_unused:UNUSED_PAD src0_sel:WORD_1 src1_sel:DWORD
	v_and_b32_sdwa v18, v53, v248 dst_sel:DWORD dst_unused:UNUSED_PAD src0_sel:WORD_1 src1_sel:DWORD
	v_and_b32_sdwa v19, v52, v248 dst_sel:DWORD dst_unused:UNUSED_PAD src0_sel:WORD_1 src1_sel:DWORD
	v_add3_u32 v17, v17, v28, s55
	s_waitcnt lgkmcnt(1)
; #define LAS __attribute__((address_space(3)))
; __device__ __forceinline__ unsigned pk2(float lo, float hi) { return f2bf(lo) | (f2bf(hi) << 16); }
; __device__ __forceinline__ void memattn_unit(LAS unsigned char* lds, const bf16* PROJ, const bf16* MKVl, bf16* BR, int b, int hd, int qblk, int tid) {
;     ...
;     for (int c = 0; c < 4; ++c) { f32x16 o;
; #pragma unroll
;         for (int i = 0; i < 16; ++i) o[i] = 0.f;
; #pragma unroll
;         for (int ks = 0; ks < 16; ++ks) {
;             const v4i16_t lo = __builtin_amdgcn_ds_read_tr16_b64_v4i16((LAS v4i16_t*)(vimg + kv_off(16u * ks + 8u * hh + q4, 4u * c + 2u * blk + (p >> 1)) + 8u * (p & 1u)));
;             const v4i16_t hi = __builtin_amdgcn_ds_read_tr16_b64_v4i16((LAS v4i16_t*)(vimg + kv_off(16u * ks + 8u * hh + 4u + q4, 4u * c + 2u * blk + (p >> 1)) + 8u * (p & 1u)));
;             const bf16x8 a = __builtin_shufflevector(lo, hi, 0, 1, 2, 3, 4, 5, 6, 7);
;             o = __builtin_amdgcn_mfma_f32_32x32x16_bf16(a, Bp[ks], o, 0, 0, 0); if ((ks & 3) == 3) __builtin_amdgcn_sched_barrier(0); }
; #pragma unroll
;         for (int i4 = 0; i4 < 4; ++i4) { v2u w; w.x = pk2(o[4 * i4] * inv, o[4 * i4 + 1] * inv); w.y = pk2(o[4 * i4 + 2] * inv, o[4 * i4 + 3] * inv);
;             *(v2u*)(orow + 32 * c + 8 * i4 + 4 * hh) = w; } }
;     __syncthreads();
; __global__ void __launch_bounds__(NWAVES * 64, 2) fwd(Args args) {
;     ...
;             for (int u = F.bx; u < NB * 4 * (T / 256); u += F.G) { const int qblk = u % (T / 256), hd = (u / (T / 256)) & 3, b = u / (4 * (T / 256));
;                 memattn_unit(F.lds, PROJ, MKV + (size_t)l * 512 * 1024, BR, b, hd, qblk, F.tid); }
	v_mfma_f32_32x32x16_bf16 v[0:15], v[20:23], v[56:59], v[0:15]
	v_add3_u32 v16, v16, v29, s55
	v_add3_u32 v19, v52, v19, s55
	v_add3_u32 v18, v53, v18, s55
	v_and_b32_e32 v17, 0xffff0000, v17
	v_and_b32_e32 v16, 0xffff0000, v16
	v_or_b32_sdwa v17, v17, v18 dst_sel:DWORD dst_unused:UNUSED_PAD src0_sel:DWORD src1_sel:WORD_1
	v_or_b32_sdwa v16, v16, v19 dst_sel:DWORD dst_unused:UNUSED_PAD src0_sel:DWORD src1_sel:WORD_1
	global_store_dwordx2 v[96:97], v[16:17], off offset:3248
	s_waitcnt lgkmcnt(0)
	v_mfma_f32_32x32x16_bf16 v[0:15], v[24:27], v[40:43], v[0:15]
	ds_read_b64_tr_b16 v[18:19], v100 offset:17408
	ds_read_b64_tr_b16 v[16:17], v99 offset:16384
	ds_read_b64_tr_b16 v[20:21], v99 offset:20480
	ds_read_b64_tr_b16 v[24:25], v99 offset:24576
	ds_read_b64_tr_b16 v[28:29], v99 offset:28672
	ds_read_b64_tr_b16 v[22:23], v100 offset:21504
	ds_read_b64_tr_b16 v[26:27], v100 offset:25600
	ds_read_b64_tr_b16 v[30:31], v100 offset:29696
	s_waitcnt lgkmcnt(6)
	v_mfma_f32_32x32x16_bf16 v[0:15], v[16:19], v[32:35], v[0:15]
	s_waitcnt lgkmcnt(2)
	v_mfma_f32_32x32x16_bf16 v[0:15], v[20:23], v[36:39], v[0:15]
	s_waitcnt lgkmcnt(1)
	v_mfma_f32_32x32x16_bf16 v[0:15], v[24:27], v[48:51], v[0:15]
	s_waitcnt lgkmcnt(0)
	v_mfma_f32_32x32x16_bf16 v[0:15], v[28:31], v[64:67], v[0:15]
	ds_read_b64_tr_b16 v[18:19], v100 offset:33792
	ds_read_b64_tr_b16 v[16:17], v99 offset:32768
	ds_read_b64_tr_b16 v[20:21], v99 offset:36864
	ds_read_b64_tr_b16 v[24:25], v99 offset:40960
	ds_read_b64_tr_b16 v[28:29], v99 offset:45056
	ds_read_b64_tr_b16 v[22:23], v100 offset:37888
	ds_read_b64_tr_b16 v[26:27], v100 offset:41984
	ds_read_b64_tr_b16 v[30:31], v100 offset:46080
	s_waitcnt lgkmcnt(6)
	v_mfma_f32_32x32x16_bf16 v[0:15], v[16:19], v[44:47], v[0:15]
	s_waitcnt lgkmcnt(2)
	v_mfma_f32_32x32x16_bf16 v[0:15], v[20:23], v[60:63], v[0:15]
	s_waitcnt lgkmcnt(1)
	v_mfma_f32_32x32x16_bf16 v[0:15], v[24:27], v[72:75], v[0:15]
	s_waitcnt lgkmcnt(0)
	v_mfma_f32_32x32x16_bf16 v[0:15], v[28:31], v[80:83], v[0:15]
	ds_read_b64_tr_b16 v[18:19], v100 offset:50176
	ds_read_b64_tr_b16 v[16:17], v99 offset:49152
	ds_read_b64_tr_b16 v[20:21], v99 offset:53248
	ds_read_b64_tr_b16 v[24:25], v99 offset:57344
	ds_read_b64_tr_b16 v[28:29], v99 offset:61440
	ds_read_b64_tr_b16 v[22:23], v100 offset:54272
	ds_read_b64_tr_b16 v[26:27], v100 offset:58368
	ds_read_b64_tr_b16 v[30:31], v100 offset:62464
	s_waitcnt lgkmcnt(6)
	v_mfma_f32_32x32x16_bf16 v[0:15], v[16:19], v[68:71], v[0:15]
	s_waitcnt lgkmcnt(2)
	v_mfma_f32_32x32x16_bf16 v[0:15], v[20:23], v[76:79], v[0:15]
	s_waitcnt lgkmcnt(1)
	v_mfma_f32_32x32x16_bf16 v[0:15], v[24:27], v[84:87], v[0:15]
	s_waitcnt lgkmcnt(0)
	v_mfma_f32_32x32x16_bf16 v[0:15], v[28:31], v[88:91], v[0:15]
	s_nop 11
	v_mov_b32_e32 v16, v0
	v_mov_b32_e32 v17, v2
	v_pk_mul_f32 v[16:17], v[98:99], v[16:17] op_sel_hi:[0,1]
	v_mov_b32_e32 v2, v1
	v_pk_mul_f32 v[0:1], v[98:99], v[2:3] op_sel_hi:[0,1]
	v_and_b32_sdwa v2, v17, v248 dst_sel:DWORD dst_unused:UNUSED_PAD src0_sel:WORD_1 src1_sel:DWORD
	v_and_b32_sdwa v3, v16, v248 dst_sel:DWORD dst_unused:UNUSED_PAD src0_sel:WORD_1 src1_sel:DWORD
	v_add3_u32 v3, v16, v3, s55
	v_add3_u32 v2, v17, v2, s55
	v_and_b32_sdwa v16, v1, v248 dst_sel:DWORD dst_unused:UNUSED_PAD src0_sel:WORD_1 src1_sel:DWORD
	v_and_b32_sdwa v17, v0, v248 dst_sel:DWORD dst_unused:UNUSED_PAD src0_sel:WORD_1 src1_sel:DWORD
	v_add3_u32 v1, v1, v16, s55
	v_add3_u32 v0, v0, v17, s55
	v_and_b32_e32 v1, 0xffff0000, v1
	v_and_b32_e32 v0, 0xffff0000, v0
	v_or_b32_sdwa v1, v1, v2 dst_sel:DWORD dst_unused:UNUSED_PAD src0_sel:DWORD src1_sel:WORD_1
	v_or_b32_sdwa v0, v0, v3 dst_sel:DWORD dst_unused:UNUSED_PAD src0_sel:DWORD src1_sel:WORD_1
	global_store_dwordx2 v[96:97], v[0:1], off offset:3264
	v_mov_b32_e32 v0, v4
	v_mov_b32_e32 v1, v6
	v_pk_mul_f32 v[0:1], v[98:99], v[0:1] op_sel_hi:[0,1]
	v_mov_b32_e32 v6, v5
	v_pk_mul_f32 v[2:3], v[98:99], v[6:7] op_sel_hi:[0,1]
	v_and_b32_sdwa v4, v1, v248 dst_sel:DWORD dst_unused:UNUSED_PAD src0_sel:WORD_1 src1_sel:DWORD
	v_and_b32_sdwa v5, v0, v248 dst_sel:DWORD dst_unused:UNUSED_PAD src0_sel:WORD_1 src1_sel:DWORD
	v_add3_u32 v0, v0, v5, s55
	v_add3_u32 v1, v1, v4, s55
	v_and_b32_sdwa v4, v3, v248 dst_sel:DWORD dst_unused:UNUSED_PAD src0_sel:WORD_1 src1_sel:DWORD
	v_and_b32_sdwa v5, v2, v248 dst_sel:DWORD dst_unused:UNUSED_PAD src0_sel:WORD_1 src1_sel:DWORD
	v_add3_u32 v3, v3, v4, s55
	v_add3_u32 v2, v2, v5, s55
	v_and_b32_e32 v3, 0xffff0000, v3
	v_and_b32_e32 v2, 0xffff0000, v2
	v_or_b32_sdwa v1, v3, v1 dst_sel:DWORD dst_unused:UNUSED_PAD src0_sel:DWORD src1_sel:WORD_1
	v_or_b32_sdwa v0, v2, v0 dst_sel:DWORD dst_unused:UNUSED_PAD src0_sel:DWORD src1_sel:WORD_1
	global_store_dwordx2 v[96:97], v[0:1], off offset:3280
	v_mov_b32_e32 v0, v8
	v_mov_b32_e32 v1, v10
	v_pk_mul_f32 v[0:1], v[98:99], v[0:1] op_sel_hi:[0,1]
	v_mov_b32_e32 v10, v9
	v_pk_mul_f32 v[2:3], v[98:99], v[10:11] op_sel_hi:[0,1]
	v_and_b32_sdwa v4, v1, v248 dst_sel:DWORD dst_unused:UNUSED_PAD src0_sel:WORD_1 src1_sel:DWORD
	v_and_b32_sdwa v5, v0, v248 dst_sel:DWORD dst_unused:UNUSED_PAD src0_sel:WORD_1 src1_sel:DWORD
	v_add3_u32 v0, v0, v5, s55
	v_add3_u32 v1, v1, v4, s55
	v_and_b32_sdwa v4, v3, v248 dst_sel:DWORD dst_unused:UNUSED_PAD src0_sel:WORD_1 src1_sel:DWORD
	v_and_b32_sdwa v5, v2, v248 dst_sel:DWORD dst_unused:UNUSED_PAD src0_sel:WORD_1 src1_sel:DWORD
	v_add3_u32 v3, v3, v4, s55
	v_add3_u32 v2, v2, v5, s55
	v_and_b32_e32 v3, 0xffff0000, v3
	v_and_b32_e32 v2, 0xffff0000, v2
	v_or_b32_sdwa v1, v3, v1 dst_sel:DWORD dst_unused:UNUSED_PAD src0_sel:DWORD src1_sel:WORD_1
	v_or_b32_sdwa v0, v2, v0 dst_sel:DWORD dst_unused:UNUSED_PAD src0_sel:DWORD src1_sel:WORD_1
	global_store_dwordx2 v[96:97], v[0:1], off offset:3296
	v_mov_b32_e32 v0, v12
	v_mov_b32_e32 v1, v14
	v_pk_mul_f32 v[0:1], v[98:99], v[0:1] op_sel_hi:[0,1]
	v_mov_b32_e32 v14, v13
	v_pk_mul_f32 v[2:3], v[98:99], v[14:15] op_sel_hi:[0,1]
	v_and_b32_sdwa v4, v1, v248 dst_sel:DWORD dst_unused:UNUSED_PAD src0_sel:WORD_1 src1_sel:DWORD
	v_and_b32_sdwa v5, v0, v248 dst_sel:DWORD dst_unused:UNUSED_PAD src0_sel:WORD_1 src1_sel:DWORD
	v_add3_u32 v0, v0, v5, s55
	v_add3_u32 v1, v1, v4, s55
	v_and_b32_sdwa v4, v3, v248 dst_sel:DWORD dst_unused:UNUSED_PAD src0_sel:WORD_1 src1_sel:DWORD
	v_and_b32_sdwa v5, v2, v248 dst_sel:DWORD dst_unused:UNUSED_PAD src0_sel:WORD_1 src1_sel:DWORD
	v_add3_u32 v3, v3, v4, s55
	v_add3_u32 v2, v2, v5, s55
	v_and_b32_e32 v3, 0xffff0000, v3
	v_and_b32_e32 v2, 0xffff0000, v2
	s_add_i32 s7, s7, s15
	v_or_b32_sdwa v1, v3, v1 dst_sel:DWORD dst_unused:UNUSED_PAD src0_sel:DWORD src1_sel:WORD_1
	v_or_b32_sdwa v0, v2, v0 dst_sel:DWORD dst_unused:UNUSED_PAD src0_sel:DWORD src1_sel:WORD_1
	s_cmpk_gt_i32 s7, 0xff
	global_store_dwordx2 v[96:97], v[0:1], off offset:3312
	s_barrier
	s_cbranch_scc0 .LBB0_599
